# more last-use loads marked non-temporal: x and W_in reads of the prologue, x1 reads of the router, chunk-contribution reads of the scan, ys/x1 reads of the final combine
# baseline (speedup 1.0000x reference)
; template <int MODE>
; __device__ __forceinline__ void skinny_f32(const float* X, int r0, int kbeg, const float* W, const float* lnw, bf16_t* XB, f32x16& acc, float& ssq, int lane) {
;     ...
;     SK_LOAD(a, lw, b, kbeg);
.LBB0_13:
	s_lshl_b32 s33, s35, 6
	v_add_u32_e32 v2, s33, v163
	v_ashrrev_i32_e32 v3, 31, v2
	v_readlane_b32 s36, v245, 21
	v_lshlrev_b64 v[2:3], 13, v[2:3]
	v_readlane_b32 s37, v245, 22
	v_readlane_b32 s38, v245, 23
	v_readlane_b32 s39, v245, 24
	v_lshl_add_u64 v[2:3], s[36:37], 0, v[2:3]
	v_lshl_add_u64 v[2:3], v[2:3], 0, v[114:115]
	global_load_dwordx4 v[50:53], v[2:3], off offset:48 nt
	global_load_dwordx4 v[54:57], v[2:3], off offset:32 nt
	global_load_dwordx4 v[58:61], v[2:3], off offset:16 nt
	global_load_dwordx4 v[62:65], v[2:3], off nt
	global_load_dwordx4 v[78:81], v[160:161], off offset:48
	global_load_dwordx4 v[74:77], v[160:161], off offset:32
	global_load_dwordx4 v[70:73], v[160:161], off offset:16
	global_load_dwordx4 v[66:69], v[160:161], off
	v_mov_b32_e32 v2, 0
	v_readlane_b32 s40, v245, 25
	v_readlane_b32 s41, v245, 26
	v_readlane_b32 s42, v245, 27
	v_readlane_b32 s43, v245, 28
	v_readlane_b32 s44, v245, 29
	v_readlane_b32 s45, v245, 30
	v_readlane_b32 s46, v245, 31
	v_readlane_b32 s47, v245, 32
	v_readlane_b32 s48, v245, 33
	v_readlane_b32 s49, v245, 34
	v_readlane_b32 s50, v245, 35
	v_readlane_b32 s51, v245, 36
	s_and_saveexec_b64 s[0:1], s[2:3]
	s_cbranch_execz .LBB0_15
	global_load_dword v2, v[120:121], off

; template <int MODE>
; __device__ __forceinline__ void skinny_f32(const float* X, int r0, int kbeg, const float* W, const float* lnw, bf16_t* XB, f32x16& acc, float& ssq, int lane) {
;     ...
;     SK_LOAD(a, lw, b, kbeg);
; #pragma unroll 1
;     for (int kb = kbeg; kb < kbeg + 512; kb += 32) {
;         const int k0 = kb + 16 * kk;
;         if (kb + 32 < kbeg + 512) SK_LOAD(na, nlw, nb, kb + 32);
.LBB0_46:
	s_add_i32 s36, s36, 32
	s_cmp_ge_u32 s36, s19
	s_cselect_b64 s[26:27], -1, 0
	s_and_b64 vcc, exec, s[26:27]
	s_cbranch_vccnz .LBB0_80
	v_lshl_add_u64 v[34:35], v[164:165], 0, v[116:117]
	v_lshl_add_u64 v[36:37], s[0:1], 0, v[116:117]
	global_load_dwordx4 v[82:85], v[34:35], off offset:176 nt
	global_load_dwordx4 v[86:89], v[34:35], off offset:160 nt
	global_load_dwordx4 v[90:93], v[34:35], off offset:144 nt
	global_load_dwordx4 v[94:97], v[34:35], off offset:128 nt
	global_load_dwordx4 v[98:101], v[36:37], off offset:176
	global_load_dwordx4 v[102:105], v[36:37], off offset:160
	global_load_dwordx4 v[106:109], v[36:37], off offset:144
	global_load_dwordx4 v[110:113], v[36:37], off offset:128
	v_mov_b32_e32 v35, 0
	v_mov_b32_e32 v34, 0
	s_and_saveexec_b64 s[28:29], s[2:3]
	s_cbranch_execz .LBB0_49
	v_lshl_add_u64 v[36:37], v[170:171], 0, v[118:119]
	global_load_dword v34, v[36:37], off

; #define LAS __attribute__((address_space(3)))
; __device__ __forceinline__ unsigned cvt_pk_bf16(float lo, float hi) { const f32x2_t v = {lo, hi}; return __builtin_bit_cast(unsigned, __builtin_convertvector(v, bf16x2_t)); }
; __device__ __forceinline__ void p0_transpose_item_bf16(const float* W, int ldw, int k0, int n0, bf16_t* WT, int K, int drow0, const float* sc, LAS unsigned char* tile, int lane) {
;     const int kq = lane >> 4, nq = lane & 15;
;     const float* src = W + (size_t)(k0 + 4 * kq) * ldw + n0 + 4 * nq;
; #pragma unroll
;     for (int hb = 0; hb < 2; ++hb) {
;         f32x4 v[4][4], sv[4];
;         const float* scp = sc ? sc + k0 + 64 * hb + 4 * kq : src;
; #pragma unroll
;         for (int i = 0; i < 4; ++i) sv[i] = *(const f32x4*)(scp + (sc ? 16 * i : 0));
; #pragma unroll
;         for (int i = 0; i < 4; ++i)
; #pragma unroll
;             for (int j = 0; j < 4; ++j) v[i][j] = *(const f32x4*)(src + (size_t)(64 * hb + 16 * i + j) * ldw);
; #pragma unroll
;         for (int i = 0; i < 4; ++i) {
;             const f32x4 s4 = sc ? sv[i] : (f32x4){1.f, 1.f, 1.f, 1.f};
; #pragma unroll
;             for (int nn = 0; nn < 4; ++nn) { u32x2 t; t.x = cvt_pk_bf16(v[i][0][nn] * s4[0], v[i][1][nn] * s4[1]); t.y = cvt_pk_bf16(v[i][2][nn] * s4[2], v[i][3][nn] * s4[3]);
;                 const int chunk = 2 * (4 * hb + i) + (kq >> 1);
;                 *(LAS u32x2*)(tile + (4 * nq + nn) * 256 + ((chunk ^ nq) << 4) + ((kq & 1) << 3)) = t; }
;         }
; __device__ __forceinline__ void p0_prologue(const Params& p, Frame& F) {
;     ...
;         for (int it = gw; it < I_IN; it += NGW) {
.LBB0_91:
	s_mul_hi_i32 s0, s6, 0x92492493
	s_add_i32 s0, s0, s6
	s_lshr_b32 s1, s0, 31
	s_ashr_i32 s0, s0, 6
	s_add_i32 s0, s0, s1
	s_lshl_b32 s4, s0, 7
	s_mulk_i32 s0, 0xe400
	s_add_i32 s0, s10, s0
	v_or_b32_e32 v2, s4, v120
	v_mad_i64_i32 v[2:3], s[40:41], v2, s12, v[114:115]
	s_ashr_i32 s1, s0, 31
	v_lshl_add_u64 v[2:3], s[0:1], 2, v[2:3]
	v_lshl_add_u64 v[116:117], v[2:3], 0, v[108:109]
	v_add_co_u32_e32 v2, vcc, s13, v116
	s_ashr_i32 s5, s4, 31
	s_nop 0
	v_addc_co_u32_e32 v3, vcc, 0, v117, vcc
	global_load_dwordx4 v[60:63], v[116:117], off nt
	global_load_dwordx4 v[64:67], v[2:3], off offset:32 nt
	v_add_co_u32_e32 v2, vcc, s14, v116
	v_lshl_add_u64 v[118:119], s[4:5], 2, v[110:111]
	s_nop 0
	v_addc_co_u32_e32 v3, vcc, 0, v117, vcc
	v_add_co_u32_e32 v4, vcc, s15, v116
	v_mov_b32_e32 v36, 1.0
	s_nop 0
	v_addc_co_u32_e32 v5, vcc, 0, v117, vcc
	global_load_dwordx4 v[68:71], v[2:3], off offset:64 nt
	global_load_dwordx4 v[72:75], v[4:5], off offset:96 nt
	v_add_co_u32_e32 v2, vcc, s16, v116
	v_mov_b32_e32 v37, 1.0
	s_nop 0
	v_addc_co_u32_e32 v3, vcc, 0, v117, vcc
	v_add_co_u32_e32 v4, vcc, s17, v116
	v_mov_b32_e32 v38, 1.0
	s_nop 0
	v_addc_co_u32_e32 v5, vcc, 0, v117, vcc
	global_load_dwordx4 v[44:47], v[2:3], off offset:512 nt
	global_load_dwordx4 v[48:51], v[4:5], off offset:544 nt
	v_add_co_u32_e32 v2, vcc, s18, v116
	v_mov_b32_e32 v39, 1.0
	s_nop 0
	v_addc_co_u32_e32 v3, vcc, 0, v117, vcc
	v_add_co_u32_e32 v4, vcc, s19, v116
	v_mov_b32_e32 v40, 1.0
	s_nop 0
	v_addc_co_u32_e32 v5, vcc, 0, v117, vcc
	global_load_dwordx4 v[52:55], v[2:3], off offset:576 nt
	global_load_dwordx4 v[56:59], v[4:5], off offset:608 nt
	v_add_co_u32_e32 v2, vcc, s20, v116
	v_mov_b32_e32 v41, 1.0
	s_nop 0
	v_addc_co_u32_e32 v3, vcc, 0, v117, vcc
	v_add_co_u32_e32 v4, vcc, s21, v116
	v_mov_b32_e32 v42, 1.0
	s_nop 0
	v_addc_co_u32_e32 v5, vcc, 0, v117, vcc
	global_load_dwordx4 v[12:15], v[2:3], off offset:1024 nt
	global_load_dwordx4 v[16:19], v[4:5], off offset:1056 nt
	v_add_co_u32_e32 v2, vcc, s22, v116
	v_mov_b32_e32 v43, 1.0
	s_nop 0
	v_addc_co_u32_e32 v3, vcc, 0, v117, vcc
	v_add_co_u32_e32 v4, vcc, s23, v116
	v_mov_b32_e32 v76, 1.0
	s_nop 0
	v_addc_co_u32_e32 v5, vcc, 0, v117, vcc
	global_load_dwordx4 v[28:31], v[2:3], off offset:1088 nt
	global_load_dwordx4 v[32:35], v[4:5], off offset:1120 nt
	v_add_co_u32_e32 v2, vcc, s24, v116
	v_mov_b32_e32 v77, 1.0
	s_nop 0
	v_addc_co_u32_e32 v3, vcc, 0, v117, vcc
	v_add_co_u32_e32 v8, vcc, 0x157000, v116
	v_mov_b32_e32 v78, 1.0
	s_nop 0
	v_addc_co_u32_e32 v9, vcc, 0, v117, vcc
	global_load_dwordx4 v[4:7], v[2:3], off offset:1536 nt
	s_nop 0
	global_load_dwordx4 v[8:11], v[8:9], off offset:1568 nt
	v_add_co_u32_e32 v2, vcc, 0x15e000, v116
	v_mov_b32_e32 v79, 1.0
	s_nop 0
	v_addc_co_u32_e32 v3, vcc, 0, v117, vcc
	v_add_co_u32_e32 v24, vcc, 0x165000, v116
	v_mov_b32_e32 v80, 1.0
	s_nop 0
	v_addc_co_u32_e32 v25, vcc, 0, v117, vcc
	global_load_dwordx4 v[20:23], v[2:3], off offset:1600 nt
	s_nop 0
	global_load_dwordx4 v[24:27], v[24:25], off offset:1632 nt
	v_mov_b32_e32 v2, 1.0
	s_and_b64 vcc, exec, s[2:3]
	v_mov_b32_e32 v81, 1.0
	v_mov_b32_e32 v82, 1.0
	v_mov_b32_e32 v83, 1.0
	s_cbranch_vccnz .LBB0_93
	global_load_dwordx4 v[36:39], v[118:119], off offset:192 nt
	global_load_dwordx4 v[40:43], v[118:119], off offset:128 nt
	global_load_dwordx4 v[76:79], v[118:119], off offset:64 nt
	global_load_dwordx4 v[80:83], v[118:119], off nt
.LBB0_93:
	s_waitcnt vmcnt(15)
	v_mov_b32_e32 v84, v60
	s_waitcnt vmcnt(14)
	v_mov_b32_e32 v85, v64
	s_waitcnt vmcnt(13)
	v_mov_b32_e32 v86, v68
	s_waitcnt vmcnt(12)
	v_mov_b32_e32 v87, v72
	v_mov_b32_e32 v64, v61
	v_mov_b32_e32 v72, v69
	s_waitcnt vmcnt(0)
	v_pk_mul_f32 v[84:85], v[84:85], v[80:81]
	v_pk_mul_f32 v[86:87], v[86:87], v[82:83]
	v_pk_mul_f32 v[60:61], v[64:65], v[80:81]
	v_pk_mul_f32 v[64:65], v[72:73], v[82:83]
	v_cvt_pk_bf16_f32 v84, v84, v85
	v_cvt_pk_bf16_f32 v85, v86, v87
	v_cvt_pk_bf16_f32 v60, v60, v61
	v_cvt_pk_bf16_f32 v61, v64, v65
	v_add_u32_e32 v3, 0x4000, v121
	ds_write2_b64 v3, v[84:85], v[60:61] offset1:32
	v_mov_b32_e32 v60, v62
	v_mov_b32_e32 v61, v66
	v_mov_b32_e32 v64, v70
	v_mov_b32_e32 v65, v74
	v_pk_mul_f32 v[60:61], v[60:61], v[80:81]
	v_pk_mul_f32 v[64:65], v[64:65], v[82:83]
	v_mov_b32_e32 v66, v63
	v_mov_b32_e32 v74, v71
	v_cvt_pk_bf16_f32 v60, v60, v61
	v_cvt_pk_bf16_f32 v61, v64, v65
	v_pk_mul_f32 v[62:63], v[66:67], v[80:81]
	v_pk_mul_f32 v[64:65], v[74:75], v[82:83]
	v_cvt_pk_bf16_f32 v62, v62, v63
	v_cvt_pk_bf16_f32 v63, v64, v65
	ds_write2_b64 v3, v[60:61], v[62:63] offset0:64 offset1:96
	v_mov_b32_e32 v60, v44
	v_mov_b32_e32 v61, v48
	v_mov_b32_e32 v62, v52
	v_mov_b32_e32 v63, v56
	v_mov_b32_e32 v48, v45
	v_mov_b32_e32 v56, v53
	v_pk_mul_f32 v[60:61], v[60:61], v[76:77]
	v_pk_mul_f32 v[62:63], v[62:63], v[78:79]
	v_pk_mul_f32 v[44:45], v[48:49], v[76:77]
	v_pk_mul_f32 v[48:49], v[56:57], v[78:79]
	v_cvt_pk_bf16_f32 v60, v60, v61
	v_cvt_pk_bf16_f32 v61, v62, v63
	v_cvt_pk_bf16_f32 v44, v44, v45
	v_cvt_pk_bf16_f32 v45, v48, v49
	v_add_u32_e32 v3, 0x4000, v122
	ds_write2_b64 v3, v[60:61], v[44:45] offset1:32
	v_mov_b32_e32 v44, v46
	v_mov_b32_e32 v45, v50
	v_pk_mul_f32 v[44:45], v[44:45], v[76:77]
	v_mov_b32_e32 v50, v47
	v_cvt_pk_bf16_f32 v146, v44, v45
	v_mov_b32_e32 v44, v54
	v_mov_b32_e32 v45, v58
	v_pk_mul_f32 v[44:45], v[44:45], v[78:79]
	v_mov_b32_e32 v58, v55
	v_cvt_pk_bf16_f32 v147, v44, v45
; #define LAS __attribute__((address_space(3)))
; __device__ __forceinline__ unsigned cvt_pk_bf16(float lo, float hi) { const f32x2_t v = {lo, hi}; return __builtin_bit_cast(unsigned, __builtin_convertvector(v, bf16x2_t)); }
; __device__ __forceinline__ void p0_transpose_item_bf16(const float* W, int ldw, int k0, int n0, bf16_t* WT, int K, int drow0, const float* sc, LAS unsigned char* tile, int lane) {
;     ...
;     for (int hb = 0; hb < 2; ++hb) {
;         f32x4 v[4][4], sv[4];
;         const float* scp = sc ? sc + k0 + 64 * hb + 4 * kq : src;
; #pragma unroll
;         for (int i = 0; i < 4; ++i) sv[i] = *(const f32x4*)(scp + (sc ? 16 * i : 0));
; #pragma unroll
;         for (int i = 0; i < 4; ++i)
; #pragma unroll
;             for (int j = 0; j < 4; ++j) v[i][j] = *(const f32x4*)(src + (size_t)(64 * hb + 16 * i + j) * ldw);
; #pragma unroll
;         for (int i = 0; i < 4; ++i) {
;             const f32x4 s4 = sc ? sv[i] : (f32x4){1.f, 1.f, 1.f, 1.f};
; #pragma unroll
;             for (int nn = 0; nn < 4; ++nn) { u32x2 t; t.x = cvt_pk_bf16(v[i][0][nn] * s4[0], v[i][1][nn] * s4[1]); t.y = cvt_pk_bf16(v[i][2][nn] * s4[2], v[i][3][nn] * s4[3]);
;                 const int chunk = 2 * (4 * hb + i) + (kq >> 1);
;                 *(LAS u32x2*)(tile + (4 * nq + nn) * 256 + ((chunk ^ nq) << 4) + ((kq & 1) << 3)) = t; }
;         }
	v_pk_mul_f32 v[44:45], v[50:51], v[76:77]
	s_nop 0
	v_cvt_pk_bf16_f32 v148, v44, v45
	v_pk_mul_f32 v[44:45], v[58:59], v[78:79]
	s_nop 0
	v_cvt_pk_bf16_f32 v149, v44, v45
	v_add_co_u32_e32 v44, vcc, s25, v116
	s_nop 1
	v_addc_co_u32_e32 v45, vcc, 0, v117, vcc
	v_add_co_u32_e32 v46, vcc, s26, v116
	s_nop 1
	v_addc_co_u32_e32 v47, vcc, 0, v117, vcc
	global_load_dwordx4 v[92:95], v[44:45], off offset:2048 nt
	global_load_dwordx4 v[96:99], v[46:47], off offset:2080 nt
	v_add_co_u32_e32 v44, vcc, s27, v116
	s_nop 1
	v_addc_co_u32_e32 v45, vcc, 0, v117, vcc
	v_add_co_u32_e32 v46, vcc, s28, v116
	s_nop 1
	v_addc_co_u32_e32 v47, vcc, 0, v117, vcc
	global_load_dwordx4 v[100:103], v[44:45], off offset:2112 nt
	global_load_dwordx4 v[104:107], v[46:47], off offset:2144 nt
	v_add_co_u32_e32 v44, vcc, s29, v116
	s_nop 1
	v_addc_co_u32_e32 v45, vcc, 0, v117, vcc
	v_add_co_u32_e32 v46, vcc, s30, v116
	s_nop 1
	v_addc_co_u32_e32 v47, vcc, 0, v117, vcc
	global_load_dwordx4 v[76:79], v[44:45], off offset:2560 nt
	global_load_dwordx4 v[80:83], v[46:47], off offset:2592 nt
	v_add_co_u32_e32 v44, vcc, s31, v116
	s_nop 1
	v_addc_co_u32_e32 v45, vcc, 0, v117, vcc
	v_add_co_u32_e32 v46, vcc, s33, v116
	s_nop 1
	v_addc_co_u32_e32 v47, vcc, 0, v117, vcc
	global_load_dwordx4 v[84:87], v[44:45], off offset:2624 nt
	global_load_dwordx4 v[88:91], v[46:47], off offset:2656 nt
	v_add_co_u32_e32 v44, vcc, s34, v116
	s_nop 1
	v_addc_co_u32_e32 v45, vcc, 0, v117, vcc
	v_add_co_u32_e32 v46, vcc, s35, v116
	s_nop 1
	v_addc_co_u32_e32 v47, vcc, 0, v117, vcc
	global_load_dwordx4 v[60:63], v[44:45], off offset:3072 nt
	global_load_dwordx4 v[64:67], v[46:47], off offset:3104 nt
	v_add_co_u32_e32 v44, vcc, s36, v116
	s_nop 1
	v_addc_co_u32_e32 v45, vcc, 0, v117, vcc
	v_add_co_u32_e32 v46, vcc, s37, v116
	s_nop 1
	v_addc_co_u32_e32 v47, vcc, 0, v117, vcc
	global_load_dwordx4 v[68:71], v[44:45], off offset:3136 nt
	global_load_dwordx4 v[72:75], v[46:47], off offset:3168 nt
	v_add_co_u32_e32 v44, vcc, s38, v116
	s_nop 1
	v_addc_co_u32_e32 v45, vcc, 0, v117, vcc
	v_add_co_u32_e32 v48, vcc, 0x317000, v116
	s_nop 1
	v_addc_co_u32_e32 v49, vcc, 0, v117, vcc
	v_add_co_u32_e32 v52, vcc, 0x31e000, v116
	global_load_dwordx4 v[44:47], v[44:45], off offset:3584 nt
	s_nop 0
	global_load_dwordx4 v[48:51], v[48:49], off offset:3616 nt
	v_addc_co_u32_e32 v53, vcc, 0, v117, vcc
	v_add_co_u32_e32 v56, vcc, 0x325000, v116
	v_mov_b32_e32 v116, v12
	s_nop 0
	v_addc_co_u32_e32 v57, vcc, 0, v117, vcc
	global_load_dwordx4 v[52:55], v[52:53], off offset:3648 nt
	s_nop 0
	global_load_dwordx4 v[56:59], v[56:57], off offset:3680 nt
	ds_write2_b64 v3, v[146:147], v[148:149] offset0:64 offset1:96
	v_mov_b32_e32 v117, v16
	v_mov_b32_e32 v146, v28
	v_mov_b32_e32 v147, v32
	v_mov_b32_e32 v16, v13
	v_mov_b32_e32 v32, v29
	v_pk_mul_f32 v[116:117], v[116:117], v[40:41]
	v_pk_mul_f32 v[146:147], v[146:147], v[42:43]
	v_pk_mul_f32 v[12:13], v[16:17], v[40:41]
	v_pk_mul_f32 v[16:17], v[32:33], v[42:43]
	v_cvt_pk_bf16_f32 v116, v116, v117
	v_cvt_pk_bf16_f32 v117, v146, v147
	v_cvt_pk_bf16_f32 v12, v12, v13
	v_cvt_pk_bf16_f32 v13, v16, v17
	v_add_u32_e32 v3, 0x4000, v123
	ds_write2_b64 v3, v[116:117], v[12:13] offset1:32
	v_mov_b32_e32 v12, v14
	v_mov_b32_e32 v13, v18
	v_mov_b32_e32 v16, v30
	v_mov_b32_e32 v17, v34
	v_pk_mul_f32 v[12:13], v[12:13], v[40:41]
	v_pk_mul_f32 v[16:17], v[16:17], v[42:43]
	v_mov_b32_e32 v18, v15
	v_mov_b32_e32 v34, v31
	v_cvt_pk_bf16_f32 v12, v12, v13
	v_cvt_pk_bf16_f32 v13, v16, v17
	v_pk_mul_f32 v[14:15], v[18:19], v[40:41]
	v_pk_mul_f32 v[16:17], v[34:35], v[42:43]
	v_cvt_pk_bf16_f32 v14, v14, v15
	v_cvt_pk_bf16_f32 v15, v16, v17
	ds_write2_b64 v3, v[12:13], v[14:15] offset0:64 offset1:96
	v_mov_b32_e32 v12, v4
	v_mov_b32_e32 v13, v8
	v_mov_b32_e32 v14, v20
	v_mov_b32_e32 v15, v24
	v_mov_b32_e32 v8, v5
	v_mov_b32_e32 v24, v21
	v_pk_mul_f32 v[12:13], v[12:13], v[36:37]
	v_pk_mul_f32 v[14:15], v[14:15], v[38:39]
	v_pk_mul_f32 v[4:5], v[8:9], v[36:37]
	v_pk_mul_f32 v[8:9], v[24:25], v[38:39]
	v_cvt_pk_bf16_f32 v12, v12, v13
	v_cvt_pk_bf16_f32 v13, v14, v15
	v_cvt_pk_bf16_f32 v4, v4, v5
	v_cvt_pk_bf16_f32 v5, v8, v9
	v_add_u32_e32 v3, 0x4000, v124
	ds_write2_b64 v3, v[12:13], v[4:5] offset1:32
	v_mov_b32_e32 v4, v6
	v_mov_b32_e32 v5, v10
	v_mov_b32_e32 v8, v22
	v_mov_b32_e32 v9, v26
	v_pk_mul_f32 v[4:5], v[4:5], v[36:37]
	v_pk_mul_f32 v[8:9], v[8:9], v[38:39]
	v_mov_b32_e32 v10, v7
	v_mov_b32_e32 v26, v23
	v_cvt_pk_bf16_f32 v4, v4, v5
	v_cvt_pk_bf16_f32 v5, v8, v9
	v_pk_mul_f32 v[6:7], v[10:11], v[36:37]
	v_pk_mul_f32 v[8:9], v[26:27], v[38:39]
	v_cvt_pk_bf16_f32 v6, v6, v7
	v_cvt_pk_bf16_f32 v7, v8, v9
	ds_write2_b64 v3, v[4:5], v[6:7] offset0:64 offset1:96
	s_and_b64 vcc, exec, s[2:3]
	v_mov_b32_e32 v3, 1.0
	v_mov_b32_e32 v4, 1.0
	v_mov_b32_e32 v5, 1.0
	v_mov_b32_e32 v6, 1.0
	v_mov_b32_e32 v7, 1.0
	v_mov_b32_e32 v8, 1.0
	v_mov_b32_e32 v9, 1.0
	v_mov_b32_e32 v10, 1.0
	v_mov_b32_e32 v11, 1.0
	v_mov_b32_e32 v12, 1.0
	v_mov_b32_e32 v13, 1.0
	v_mov_b32_e32 v14, 1.0
	v_mov_b32_e32 v15, 1.0
	v_mov_b32_e32 v16, 1.0
	v_mov_b32_e32 v17, 1.0
	s_cbranch_vccnz .LBB0_90
	global_load_dwordx4 v[2:5], v[118:119], off offset:448 nt
	global_load_dwordx4 v[6:9], v[118:119], off offset:384 nt
	global_load_dwordx4 v[10:13], v[118:119], off offset:320 nt
	global_load_dwordx4 v[14:17], v[118:119], off offset:256 nt
	s_branch .LBB0_90

; __device__ __forceinline__ void p2_scan(const Params& p, Frame& F) {
;     ...
;             for (int cb = 0; cb < NCHUNK; cb += 16) {
;                 u32x2 d[16]; float gl[16], ml[16]; f32x4 dnv[16];
; #pragma unroll
;                 for (int j = 0; j < 16; ++j) { d[j] = *(const u32x2*)(dC + (size_t)(cb + j) * 128); gl[j] = ms[(cb + j) * 4]; ml[j] = ms[(cb + j) * 4 + 1]; }
; #pragma unroll
;                 for (int j = 0; j < 16; ++j) dnv[j] = (f32x4){0.f, 0.f, 0.f, 0.f};
;                 if (do_n) {
; #pragma unroll
;                     for (int j = 0; j < 16; ++j) dnv[j] = *(const f32x4*)(dn + (cb + j) * 128);
;                 }
.LBB0_393:
	v_lshl_add_u64 v[8:9], s[96:97], 0, v[78:79]
	v_add_co_u32_e32 v8, vcc, 0x59800000, v8
	v_lshl_add_u64 v[10:11], s[96:97], 0, v[76:77]
	s_nop 0
	v_addc_co_u32_e32 v9, vcc, 0, v9, vcc
	v_add_co_u32_e32 v10, vcc, 0x900000, v10
	v_lshl_add_u64 v[84:85], s[96:97], 0, v[80:81]
	s_nop 0
	v_addc_co_u32_e32 v11, vcc, 0, v11, vcc
	global_load_dwordx2 v[150:151], v[8:9], off nt
	global_load_dwordx2 v[142:143], v[8:9], off offset:256 nt
	global_load_dwordx2 v[138:139], v[8:9], off offset:512 nt
	global_load_dwordx2 v[134:135], v[8:9], off offset:768 nt
	global_load_dwordx2 v[98:99], v[10:11], off nt
	global_load_dwordx2 v[148:149], v[10:11], off offset:16 nt
	global_load_dwordx2 v[140:141], v[10:11], off offset:32 nt
	global_load_dwordx2 v[136:137], v[10:11], off offset:48 nt
	global_load_dwordx2 v[130:131], v[8:9], off offset:1024 nt
	global_load_dwordx2 v[126:127], v[8:9], off offset:1280 nt
	global_load_dwordx2 v[122:123], v[8:9], off offset:1536 nt
	global_load_dwordx2 v[118:119], v[8:9], off offset:1792 nt
	global_load_dwordx2 v[132:133], v[10:11], off offset:64 nt
	global_load_dwordx2 v[128:129], v[10:11], off offset:80 nt
	global_load_dwordx2 v[124:125], v[10:11], off offset:96 nt
	global_load_dwordx2 v[120:121], v[10:11], off offset:112 nt
	global_load_dwordx2 v[114:115], v[8:9], off offset:2048 nt
	global_load_dwordx2 v[110:111], v[8:9], off offset:2304 nt
	global_load_dwordx2 v[106:107], v[8:9], off offset:2560 nt
	global_load_dwordx2 v[102:103], v[8:9], off offset:2816 nt
	global_load_dwordx2 v[116:117], v[10:11], off offset:128 nt
	global_load_dwordx2 v[112:113], v[10:11], off offset:144 nt
	global_load_dwordx2 v[108:109], v[10:11], off offset:160 nt
	global_load_dwordx2 v[104:105], v[10:11], off offset:176 nt
	global_load_dwordx2 v[96:97], v[8:9], off offset:3072 nt
	global_load_dwordx2 v[92:93], v[8:9], off offset:3328 nt
	global_load_dwordx2 v[88:89], v[8:9], off offset:3584 nt
	global_load_dwordx2 v[82:83], v[8:9], off offset:3840 nt
	global_load_dwordx2 v[100:101], v[10:11], off offset:192 nt
	global_load_dwordx2 v[94:95], v[10:11], off offset:208 nt
	global_load_dwordx2 v[90:91], v[10:11], off offset:224 nt
	global_load_dwordx2 v[86:87], v[10:11], off offset:240 nt
	v_mov_b32_e32 v8, 0
	v_mov_b32_e32 v9, 0
	v_mov_b32_e32 v10, 0
	v_mov_b32_e32 v11, 0
	v_mov_b32_e32 v12, 0
	v_mov_b32_e32 v13, 0
	v_mov_b32_e32 v14, 0
	v_mov_b32_e32 v15, 0
	v_mov_b32_e32 v16, 0
	v_mov_b32_e32 v17, 0
	v_mov_b32_e32 v18, 0
	v_mov_b32_e32 v19, 0
	v_mov_b32_e32 v20, 0
	v_mov_b32_e32 v21, 0
	v_mov_b32_e32 v22, 0
	v_mov_b32_e32 v23, 0
	v_mov_b32_e32 v24, 0
	v_mov_b32_e32 v25, 0
	v_mov_b32_e32 v26, 0
	v_mov_b32_e32 v27, 0
	v_mov_b32_e32 v28, 0
	v_mov_b32_e32 v29, 0
	v_mov_b32_e32 v30, 0
	v_mov_b32_e32 v31, 0
	v_mov_b32_e32 v32, 0
	v_mov_b32_e32 v33, 0
	v_mov_b32_e32 v34, 0
	v_mov_b32_e32 v35, 0
	v_mov_b32_e32 v36, 0
	v_mov_b32_e32 v37, 0
	v_mov_b32_e32 v38, 0
	v_mov_b32_e32 v39, 0
	v_mov_b32_e32 v40, 0
	v_mov_b32_e32 v41, 0
	v_mov_b32_e32 v42, 0
	v_mov_b32_e32 v43, 0
	v_mov_b32_e32 v44, 0
	v_mov_b32_e32 v45, 0
	v_mov_b32_e32 v46, 0
	v_mov_b32_e32 v47, 0
	v_mov_b32_e32 v48, 0
	v_mov_b32_e32 v49, 0
	v_mov_b32_e32 v50, 0
	v_mov_b32_e32 v51, 0
	v_mov_b32_e32 v52, 0
	v_mov_b32_e32 v53, 0
	v_mov_b32_e32 v54, 0
	v_mov_b32_e32 v55, 0
	v_mov_b32_e32 v56, 0
	v_mov_b32_e32 v57, 0
	v_mov_b32_e32 v58, 0
	v_mov_b32_e32 v59, 0
	v_mov_b32_e32 v60, 0
	v_mov_b32_e32 v61, 0
	v_mov_b32_e32 v62, 0
	v_mov_b32_e32 v63, 0
	v_mov_b32_e32 v64, 0
	v_mov_b32_e32 v65, 0
	v_mov_b32_e32 v66, 0
	v_mov_b32_e32 v67, 0
	v_mov_b32_e32 v68, 0
	v_mov_b32_e32 v69, 0
	v_mov_b32_e32 v70, 0
	v_mov_b32_e32 v71, 0
	s_and_saveexec_b64 s[22:23], s[2:3]
	s_cbranch_execz .LBB0_395
	v_add_co_u32_e32 v8, vcc, 0x800000, v84
	s_nop 1
	v_addc_co_u32_e32 v9, vcc, 0, v85, vcc
	global_load_dwordx4 v[68:71], v[8:9], off
	global_load_dwordx4 v[64:67], v[8:9], off offset:512
	global_load_dwordx4 v[60:63], v[8:9], off offset:1024
	global_load_dwordx4 v[56:59], v[8:9], off offset:1536
	global_load_dwordx4 v[52:55], v[8:9], off offset:2048
	global_load_dwordx4 v[48:51], v[8:9], off offset:2560
	global_load_dwordx4 v[44:47], v[8:9], off offset:3072
	global_load_dwordx4 v[40:43], v[8:9], off offset:3584
	v_add_co_u32_e32 v8, vcc, 0x801000, v84
	s_nop 1
	v_addc_co_u32_e32 v9, vcc, 0, v85, vcc
	global_load_dwordx4 v[36:39], v[8:9], off
	global_load_dwordx4 v[32:35], v[8:9], off offset:512
	global_load_dwordx4 v[28:31], v[8:9], off offset:1024
	global_load_dwordx4 v[24:27], v[8:9], off offset:1536
	global_load_dwordx4 v[20:23], v[8:9], off offset:2048
	global_load_dwordx4 v[16:19], v[8:9], off offset:2560
	global_load_dwordx4 v[12:15], v[8:9], off offset:3072
	s_nop 0
	global_load_dwordx4 v[8:11], v[8:9], off offset:3584

; __device__ __forceinline__ unsigned cvt_pk_bf16(float lo, float hi) { const f32x2_t v = {lo, hi}; return __builtin_bit_cast(unsigned, __builtin_convertvector(v, bf16x2_t)); }
; __device__ __forceinline__ float bflo(unsigned w) { return __uint_as_float(w << 16); }
; __device__ __forceinline__ float bfhi(unsigned w) { return __uint_as_float(w & 0xffff0000u); }
; __device__ __forceinline__ void p2_scan(const Params& p, Frame& F) {
;     ...
;             const int sh = gid >> 12, rem = gid & 4095;
;             const bf16_t* dS = (const bf16_t*)(ws + WS_DS) + (size_t)(sh * 128 + (rem >> 5)) * 16384 + (rem & 31) * 4;
;             const float* dv = (const float*)(ws + WS_DVEC) + (size_t)sh * 128 * 128 + (rem & 31) * 4;
;             bf16_t* so = (bf16_t*)(ws + WS_SST) + (size_t)sh * 128 * 16384 + rem * 4;
;             f32x4 run = (f32x4){0.f, 0.f, 0.f, 0.f};
; #pragma unroll 1
;             for (int cb = 0; cb < NCHUNK; cb += 16) {
;                 u32x2 d[16]; f32x4 de[16];
; #pragma unroll
;                 for (int j = 0; j < 16; ++j) { d[j] = *(const u32x2*)(dS + (size_t)(cb + j) * 128); de[j] = *(const f32x4*)(dv + (cb + j) * 128); }
; #pragma unroll
;                 for (int j = 0; j < 16; ++j) {
;                     u32x2 o; o.x = cvt_pk_bf16(run[0], run[1]); o.y = cvt_pk_bf16(run[2], run[3]);
;                     *(u32x2*)(so + (size_t)(cb + j) * 16384) = o;
;                     run = de[j] * run + (f32x4){bflo(d[j].x), bfhi(d[j].x), bflo(d[j].y), bfhi(d[j].y)};
;                 }
.LBB0_492:
	v_lshl_add_u64 v[14:15], s[96:97], 0, v[4:5]
	v_add_co_u32_e64 v48, s[0:1], s28, v14
	v_lshl_add_u64 v[20:21], s[96:97], 0, v[6:7]
	s_nop 0
	v_addc_co_u32_e64 v49, s[0:1], 0, v15, s[0:1]
	v_add_co_u32_e64 v80, s[0:1], s29, v20
	v_lshl_add_u64 v[16:17], s[96:97], 0, v[8:9]
	s_nop 0
	v_addc_co_u32_e64 v81, s[0:1], 0, v21, s[0:1]
	v_add_co_u32_e64 v82, s[0:1], s30, v20
	v_add_co_u32_e32 v16, vcc, 0x51800000, v16
	s_nop 0
	v_addc_co_u32_e64 v83, s[0:1], 0, v21, s[0:1]
	v_add_co_u32_e64 v84, s[0:1], s31, v20
	v_addc_co_u32_e32 v17, vcc, 0, v17, vcc
	s_nop 0
	v_addc_co_u32_e64 v85, s[0:1], 0, v21, s[0:1]
	v_add_co_u32_e64 v86, s[0:1], s34, v20
	v_add_co_u32_e32 v76, vcc, 0x700000, v14
	s_nop 0
	v_addc_co_u32_e64 v87, s[0:1], 0, v21, s[0:1]
	v_add_co_u32_e64 v88, s[0:1], s35, v20
	v_addc_co_u32_e32 v77, vcc, 0, v15, vcc
	s_nop 0
	v_addc_co_u32_e64 v89, s[0:1], 0, v21, s[0:1]
	v_add_co_u32_e64 v90, s[0:1], s36, v20
	v_cvt_pk_bf16_f32 v18, v10, v11
	s_nop 0
	v_addc_co_u32_e64 v91, s[0:1], 0, v21, s[0:1]
	v_add_co_u32_e64 v92, s[0:1], s37, v20
	v_cvt_pk_bf16_f32 v19, v12, v13
	s_nop 0
	v_addc_co_u32_e64 v93, s[0:1], 0, v21, s[0:1]
	v_add_co_u32_e64 v94, s[0:1], s38, v20
	s_add_i32 s4, s4, 16
	s_nop 0
	v_addc_co_u32_e64 v95, s[0:1], 0, v21, s[0:1]
	v_add_co_u32_e64 v96, s[0:1], s39, v20
	v_lshl_add_u64 v[6:7], v[6:7], 0, s[20:21]
	s_nop 0
	v_addc_co_u32_e64 v97, s[0:1], 0, v21, s[0:1]
	v_add_co_u32_e64 v98, s[0:1], s40, v20
	v_lshl_add_u64 v[8:9], v[8:9], 0, s[16:17]
	s_nop 0
	v_addc_co_u32_e64 v99, s[0:1], 0, v21, s[0:1]
	v_add_co_u32_e64 v100, s[0:1], s41, v20
	v_lshl_add_u64 v[4:5], v[4:5], 0, s[18:19]
	s_nop 0
	v_addc_co_u32_e64 v101, s[0:1], 0, v21, s[0:1]
	v_add_co_u32_e64 v102, s[0:1], s42, v20
	s_cmpk_gt_u32 s4, 0x6f
	s_nop 0
	v_addc_co_u32_e64 v103, s[0:1], 0, v21, s[0:1]
	v_add_co_u32_e64 v104, s[0:1], s43, v20
	s_nop 1
	v_addc_co_u32_e64 v105, s[0:1], 0, v21, s[0:1]
	v_add_co_u32_e64 v106, s[0:1], s44, v20
	s_nop 1
	v_addc_co_u32_e64 v107, s[0:1], 0, v21, s[0:1]
	v_add_co_u32_e64 v108, s[0:1], s45, v20
	s_nop 1
	v_addc_co_u32_e64 v109, s[0:1], 0, v21, s[0:1]
	v_add_co_u32_e64 v110, s[0:1], s46, v20
	s_nop 1
	v_addc_co_u32_e64 v111, s[0:1], 0, v21, s[0:1]
	global_load_dwordx4 v[20:23], v[48:49], off
	global_load_dwordx4 v[24:27], v[48:49], off offset:512
	global_load_dwordx4 v[28:31], v[48:49], off offset:1024
	global_load_dwordx4 v[32:35], v[48:49], off offset:1536
	global_load_dwordx4 v[36:39], v[48:49], off offset:2048
	global_load_dwordx4 v[40:43], v[48:49], off offset:2560
	global_load_dwordx4 v[44:47], v[48:49], off offset:3072
	s_nop 0
	global_load_dwordx4 v[48:51], v[48:49], off offset:3584
	s_nop 0
	global_load_dwordx2 v[112:113], v[16:17], off nt
	global_load_dwordx2 v[114:115], v[16:17], off offset:256 nt
	global_load_dwordx2 v[116:117], v[16:17], off offset:512 nt
	global_load_dwordx2 v[118:119], v[16:17], off offset:768 nt
	global_load_dwordx2 v[120:121], v[16:17], off offset:1024 nt
	global_load_dwordx2 v[122:123], v[16:17], off offset:1280 nt
	global_load_dwordx2 v[124:125], v[16:17], off offset:1536 nt
	global_load_dwordx2 v[126:127], v[16:17], off offset:1792 nt
	global_load_dwordx2 v[128:129], v[16:17], off offset:2048 nt
	global_load_dwordx2 v[130:131], v[16:17], off offset:2304 nt
	global_load_dwordx2 v[132:133], v[16:17], off offset:2560 nt
	global_load_dwordx2 v[134:135], v[16:17], off offset:2816 nt
	global_load_dwordx2 v[136:137], v[16:17], off offset:3072 nt
	global_load_dwordx2 v[138:139], v[16:17], off offset:3328 nt
	global_load_dwordx2 v[140:141], v[16:17], off offset:3584 nt
	global_load_dwordx2 v[142:143], v[16:17], off offset:3840 nt
	s_nop 0
	global_load_dwordx4 v[14:17], v[76:77], off
	global_load_dwordx4 v[52:55], v[76:77], off offset:512
	global_load_dwordx4 v[56:59], v[76:77], off offset:1024
	global_load_dwordx4 v[60:63], v[76:77], off offset:1536
	global_load_dwordx4 v[64:67], v[76:77], off offset:2048
	global_load_dwordx4 v[68:71], v[76:77], off offset:2560
	global_load_dwordx4 v[72:75], v[76:77], off offset:3072
	s_nop 0
	global_load_dwordx4 v[76:79], v[76:77], off offset:3584
	s_waitcnt vmcnt(0)
; __device__ __forceinline__ unsigned cvt_pk_bf16(float lo, float hi) { const f32x2_t v = {lo, hi}; return __builtin_bit_cast(unsigned, __builtin_convertvector(v, bf16x2_t)); }
; __device__ __forceinline__ float bflo(unsigned w) { return __uint_as_float(w << 16); }
; __device__ __forceinline__ float bfhi(unsigned w) { return __uint_as_float(w & 0xffff0000u); }
; __device__ __forceinline__ void p2_scan(const Params& p, Frame& F) {
;     ...
;                 for (int j = 0; j < 16; ++j) {
;                     u32x2 o; o.x = cvt_pk_bf16(run[0], run[1]); o.y = cvt_pk_bf16(run[2], run[3]);
;                     *(u32x2*)(so + (size_t)(cb + j) * 16384) = o;
;                     run = de[j] * run + (f32x4){bflo(d[j].x), bfhi(d[j].x), bflo(d[j].y), bfhi(d[j].y)};
;                 }
	v_lshlrev_b32_e32 v144, 16, v116
	global_store_dwordx2 v[80:81], v[18:19], off
	v_lshlrev_b32_e32 v18, 16, v112
	v_and_b32_e32 v19, 0xffff0000, v112
	v_lshlrev_b32_e32 v80, 16, v113
	v_and_b32_e32 v81, 0xffff0000, v113
	v_lshlrev_b32_e32 v112, 16, v114
	v_and_b32_e32 v113, 0xffff0000, v114
	v_lshlrev_b32_e32 v114, 16, v115
	v_and_b32_e32 v115, 0xffff0000, v115
	v_pk_fma_f32 v[12:13], v[12:13], v[16:17], v[80:81]
	v_pk_fma_f32 v[10:11], v[10:11], v[14:15], v[18:19]
	v_and_b32_e32 v145, 0xffff0000, v116
	v_lshlrev_b32_e32 v116, 16, v117
	v_and_b32_e32 v117, 0xffff0000, v117
	v_cvt_pk_bf16_f32 v14, v10, v11
	v_cvt_pk_bf16_f32 v15, v12, v13
	v_pk_fma_f32 v[12:13], v[54:55], v[12:13], v[114:115]
	v_pk_fma_f32 v[10:11], v[52:53], v[10:11], v[112:113]
	v_lshlrev_b32_e32 v146, 16, v118
	v_and_b32_e32 v147, 0xffff0000, v118
	v_lshlrev_b32_e32 v118, 16, v119
	v_and_b32_e32 v119, 0xffff0000, v119
	global_store_dwordx2 v[82:83], v[14:15], off
	v_cvt_pk_bf16_f32 v14, v10, v11
	v_cvt_pk_bf16_f32 v15, v12, v13
	v_pk_fma_f32 v[12:13], v[58:59], v[12:13], v[116:117]
	v_pk_fma_f32 v[10:11], v[56:57], v[10:11], v[144:145]
	v_lshlrev_b32_e32 v148, 16, v120
	v_and_b32_e32 v149, 0xffff0000, v120
	v_lshlrev_b32_e32 v120, 16, v121
	v_and_b32_e32 v121, 0xffff0000, v121
	global_store_dwordx2 v[84:85], v[14:15], off
	v_cvt_pk_bf16_f32 v14, v10, v11
	v_cvt_pk_bf16_f32 v15, v12, v13
	v_pk_fma_f32 v[12:13], v[62:63], v[12:13], v[118:119]
	v_pk_fma_f32 v[10:11], v[60:61], v[10:11], v[146:147]
	v_lshlrev_b32_e32 v150, 16, v122
	v_and_b32_e32 v151, 0xffff0000, v122
	v_lshlrev_b32_e32 v122, 16, v123
	v_and_b32_e32 v123, 0xffff0000, v123
	global_store_dwordx2 v[86:87], v[14:15], off
	v_cvt_pk_bf16_f32 v14, v10, v11
	v_cvt_pk_bf16_f32 v15, v12, v13
	v_pk_fma_f32 v[12:13], v[66:67], v[12:13], v[120:121]
	v_pk_fma_f32 v[10:11], v[64:65], v[10:11], v[148:149]
	v_lshlrev_b32_e32 v152, 16, v124
	v_and_b32_e32 v153, 0xffff0000, v124
	v_lshlrev_b32_e32 v124, 16, v125
	v_and_b32_e32 v125, 0xffff0000, v125
	global_store_dwordx2 v[88:89], v[14:15], off
	v_cvt_pk_bf16_f32 v14, v10, v11
	v_cvt_pk_bf16_f32 v15, v12, v13
	v_pk_fma_f32 v[12:13], v[70:71], v[12:13], v[122:123]
	v_pk_fma_f32 v[10:11], v[68:69], v[10:11], v[150:151]
	v_lshlrev_b32_e32 v154, 16, v126
	v_and_b32_e32 v155, 0xffff0000, v126
	v_lshlrev_b32_e32 v126, 16, v127
	v_and_b32_e32 v127, 0xffff0000, v127
	global_store_dwordx2 v[90:91], v[14:15], off
	v_cvt_pk_bf16_f32 v14, v10, v11
	v_cvt_pk_bf16_f32 v15, v12, v13
	v_pk_fma_f32 v[12:13], v[74:75], v[12:13], v[124:125]
	v_pk_fma_f32 v[10:11], v[72:73], v[10:11], v[152:153]
	v_lshlrev_b32_e32 v160, 16, v128
	v_and_b32_e32 v161, 0xffff0000, v128
	v_lshlrev_b32_e32 v128, 16, v129
	v_and_b32_e32 v129, 0xffff0000, v129
	global_store_dwordx2 v[92:93], v[14:15], off
	v_cvt_pk_bf16_f32 v14, v10, v11
	v_cvt_pk_bf16_f32 v15, v12, v13
	v_pk_fma_f32 v[12:13], v[78:79], v[12:13], v[126:127]
	v_pk_fma_f32 v[10:11], v[76:77], v[10:11], v[154:155]
	v_lshlrev_b32_e32 v164, 16, v130
	v_and_b32_e32 v165, 0xffff0000, v130
	v_lshlrev_b32_e32 v130, 16, v131
	v_and_b32_e32 v131, 0xffff0000, v131
	global_store_dwordx2 v[94:95], v[14:15], off
	v_cvt_pk_bf16_f32 v14, v10, v11
	v_cvt_pk_bf16_f32 v15, v12, v13
	v_pk_fma_f32 v[12:13], v[22:23], v[12:13], v[128:129]
	v_pk_fma_f32 v[10:11], v[20:21], v[10:11], v[160:161]
	v_lshlrev_b32_e32 v166, 16, v132
	v_and_b32_e32 v167, 0xffff0000, v132
	v_lshlrev_b32_e32 v132, 16, v133
	v_and_b32_e32 v133, 0xffff0000, v133
	global_store_dwordx2 v[96:97], v[14:15], off
	v_cvt_pk_bf16_f32 v14, v10, v11
	v_cvt_pk_bf16_f32 v15, v12, v13
	v_pk_fma_f32 v[12:13], v[26:27], v[12:13], v[130:131]
	v_pk_fma_f32 v[10:11], v[24:25], v[10:11], v[164:165]
	v_lshlrev_b32_e32 v168, 16, v134
	v_and_b32_e32 v169, 0xffff0000, v134
	v_lshlrev_b32_e32 v134, 16, v135
	v_and_b32_e32 v135, 0xffff0000, v135
	global_store_dwordx2 v[98:99], v[14:15], off
	v_cvt_pk_bf16_f32 v14, v10, v11
	v_cvt_pk_bf16_f32 v15, v12, v13
	v_pk_fma_f32 v[12:13], v[30:31], v[12:13], v[132:133]
	v_pk_fma_f32 v[10:11], v[28:29], v[10:11], v[166:167]
	v_lshlrev_b32_e32 v170, 16, v136
	v_and_b32_e32 v171, 0xffff0000, v136
	v_lshlrev_b32_e32 v136, 16, v137
	v_and_b32_e32 v137, 0xffff0000, v137
	global_store_dwordx2 v[100:101], v[14:15], off
	v_cvt_pk_bf16_f32 v14, v10, v11
	v_cvt_pk_bf16_f32 v15, v12, v13
	v_pk_fma_f32 v[12:13], v[34:35], v[12:13], v[134:135]
	v_pk_fma_f32 v[10:11], v[32:33], v[10:11], v[168:169]
	v_lshlrev_b32_e32 v172, 16, v138
	v_and_b32_e32 v173, 0xffff0000, v138
	v_lshlrev_b32_e32 v138, 16, v139
	v_and_b32_e32 v139, 0xffff0000, v139
	global_store_dwordx2 v[102:103], v[14:15], off
	v_cvt_pk_bf16_f32 v14, v10, v11
	v_cvt_pk_bf16_f32 v15, v12, v13
	v_pk_fma_f32 v[12:13], v[38:39], v[12:13], v[136:137]
	v_pk_fma_f32 v[10:11], v[36:37], v[10:11], v[170:171]
	v_lshlrev_b32_e32 v174, 16, v140
	v_and_b32_e32 v175, 0xffff0000, v140
	v_lshlrev_b32_e32 v140, 16, v141
	v_and_b32_e32 v141, 0xffff0000, v141
	global_store_dwordx2 v[104:105], v[14:15], off
	v_cvt_pk_bf16_f32 v14, v10, v11
	v_cvt_pk_bf16_f32 v15, v12, v13
	v_pk_fma_f32 v[12:13], v[42:43], v[12:13], v[138:139]
	v_pk_fma_f32 v[10:11], v[40:41], v[10:11], v[172:173]
	v_lshlrev_b32_e32 v176, 16, v142
	v_and_b32_e32 v177, 0xffff0000, v142
	v_lshlrev_b32_e32 v142, 16, v143
	v_and_b32_e32 v143, 0xffff0000, v143
	global_store_dwordx2 v[106:107], v[14:15], off
	v_cvt_pk_bf16_f32 v14, v10, v11
	v_cvt_pk_bf16_f32 v15, v12, v13
	v_pk_fma_f32 v[12:13], v[46:47], v[12:13], v[140:141]
	v_pk_fma_f32 v[10:11], v[44:45], v[10:11], v[174:175]
	global_store_dwordx2 v[108:109], v[14:15], off
	v_cvt_pk_bf16_f32 v14, v10, v11
	v_cvt_pk_bf16_f32 v15, v12, v13
	v_pk_fma_f32 v[12:13], v[50:51], v[12:13], v[142:143]
	v_pk_fma_f32 v[10:11], v[48:49], v[10:11], v[176:177]
	global_store_dwordx2 v[110:111], v[14:15], off
	s_cbranch_scc0 .LBB0_492
	s_branch .LBB0_388

; template <int MODE>
; __device__ __forceinline__ void skinny_f32(const float* X, int r0, int kbeg, const float* W, const float* lnw, bf16_t* XB, f32x16& acc, float& ssq, int lane) {
;     ...
;     SK_LOAD(a, lw, b, kbeg);
; #pragma unroll 1
;     for (int kb = kbeg; kb < kbeg + 512; kb += 32) {
;         const int k0 = kb + 16 * kk;
;         if (kb + 32 < kbeg + 512) SK_LOAD(na, nlw, nb, kb + 32);
.LBB0_767:
	s_lshl_b32 s67, s66, 6
	v_add_u32_e32 v2, s67, v106
	v_ashrrev_i32_e32 v3, 31, v2
	v_lshlrev_b64 v[2:3], 13, v[2:3]
	v_lshl_add_u64 v[2:3], s[12:13], 0, v[2:3]
	v_lshl_add_u64 v[2:3], v[2:3], 0, v[98:99]
	global_load_dwordx4 v[54:57], v[2:3], off nt
	global_load_dwordx4 v[62:65], v[2:3], off offset:16 nt
	global_load_dwordx4 v[58:61], v[2:3], off offset:32 nt
	global_load_dwordx4 v[18:21], v[2:3], off offset:48 nt
	global_load_dwordx4 v[78:81], v[84:85], off nt
	global_load_dwordx4 v[74:77], v[84:85], off offset:16 nt
	global_load_dwordx4 v[70:73], v[84:85], off offset:32 nt
	global_load_dwordx4 v[66:69], v[84:85], off offset:48 nt
	global_load_dword v148, v[88:89], off
	global_load_dword v147, v[88:89], off offset:128
	global_load_dword v146, v[88:89], off offset:256
	global_load_dword v145, v[88:89], off offset:384
	global_load_dword v144, v[88:89], off offset:512
	global_load_dword v143, v[88:89], off offset:640
	global_load_dword v142, v[88:89], off offset:768
	global_load_dword v141, v[88:89], off offset:896
	global_load_dword v124, v[88:89], off offset:1024
	global_load_dword v123, v[88:89], off offset:1152
	global_load_dword v122, v[88:89], off offset:1280
	global_load_dword v121, v[88:89], off offset:1408
	global_load_dword v120, v[88:89], off offset:1536
	global_load_dword v119, v[88:89], off offset:1664
	global_load_dword v118, v[88:89], off offset:1792
	global_load_dword v117, v[88:89], off offset:1920
	v_ashrrev_i32_e32 v93, 31, v92
	v_readlane_b32 s68, v245, 39
	v_lshlrev_b64 v[2:3], 13, v[92:93]
	v_readlane_b32 s74, v245, 45
	v_readlane_b32 s75, v245, 46
	v_lshl_add_u64 v[100:101], s[96:97], 0, v[2:3]
	v_mov_b64_e32 v[102:103], v[96:97]
	v_mov_b64_e32 v[104:105], v[94:95]
	s_mov_b64 s[6:7], s[74:75]
	v_mov_b32_e32 v93, 0
	s_mov_b32 s30, s34
	v_mov_b32_e32 v2, 0
	v_mov_b32_e32 v3, v83
	v_mov_b32_e32 v4, v83
	v_mov_b32_e32 v5, v83
	v_mov_b32_e32 v6, v83
	v_mov_b32_e32 v7, v83
	v_mov_b32_e32 v8, v83
	v_mov_b32_e32 v9, v83
	v_mov_b32_e32 v10, v83
	v_mov_b32_e32 v11, v83
	v_mov_b32_e32 v12, v83
	v_mov_b32_e32 v13, v83
	v_mov_b32_e32 v14, v83
	v_mov_b32_e32 v15, v83
	v_mov_b32_e32 v16, v83
	v_mov_b32_e32 v17, v83
	v_readlane_b32 s69, v245, 40
	v_readlane_b32 s70, v245, 41
	v_readlane_b32 s71, v245, 42
	v_readlane_b32 s72, v245, 43
	v_readlane_b32 s73, v245, 44
	v_readlane_b32 s76, v245, 47
	v_readlane_b32 s77, v245, 48
	v_readlane_b32 s78, v245, 49
	v_readlane_b32 s79, v245, 50
	v_readlane_b32 s80, v245, 51
	v_readlane_b32 s81, v245, 52
	v_readlane_b32 s82, v245, 53
	v_readlane_b32 s83, v245, 54
.LBB0_768:
	s_add_i32 s30, s30, 32
	s_cmp_ge_u32 s30, s36
	s_cselect_b64 s[8:9], -1, 0
	s_and_b64 vcc, exec, s[8:9]
	s_cbranch_vccnz .LBB0_770
	v_lshl_add_u64 v[22:23], v[100:101], 0, v[82:83]
	s_mov_b64 s[68:69], 0x31800080
	v_lshl_add_u64 v[34:35], v[22:23], 0, s[68:69]
	v_add_co_u32_e32 v22, vcc, 0x31800000, v22
	v_lshl_add_u64 v[50:51], s[6:7], 0, v[82:83]
	s_nop 0
	v_addc_co_u32_e32 v23, vcc, 0, v23, vcc
	v_lshl_add_u64 v[126:127], v[104:105], 0, v[86:87]
	v_lshl_add_u64 v[150:151], v[102:103], 0, v[86:87]
	global_load_dwordx4 v[30:33], v[22:23], off offset:128 nt
	s_nop 0
	global_load_dwordx4 v[22:25], v[34:35], off offset:48 nt
	global_load_dwordx4 v[26:29], v[34:35], off offset:32 nt
	s_nop 0
	global_load_dwordx4 v[34:37], v[34:35], off offset:16 nt
	s_nop 0
	global_load_dwordx4 v[38:41], v[50:51], off offset:176 nt
	global_load_dwordx4 v[42:45], v[50:51], off offset:160 nt
	global_load_dwordx4 v[46:49], v[50:51], off offset:144 nt
	s_nop 0
	global_load_dwordx4 v[50:53], v[50:51], off offset:128 nt
	s_nop 0
	global_load_dword v125, v[126:127], off
	global_load_dword v140, v[150:151], off offset:128
	global_load_dword v139, v[150:151], off offset:256
	global_load_dword v138, v[150:151], off offset:384
	global_load_dword v137, v[150:151], off offset:512
	global_load_dword v136, v[150:151], off offset:640
	global_load_dword v135, v[150:151], off offset:768
	global_load_dword v134, v[150:151], off offset:896
	global_load_dword v133, v[150:151], off offset:1024
	global_load_dword v132, v[150:151], off offset:1152
	global_load_dword v131, v[150:151], off offset:1280
	global_load_dword v130, v[150:151], off offset:1408
	global_load_dword v129, v[150:151], off offset:1536
	global_load_dword v128, v[150:151], off offset:1664
	global_load_dword v127, v[150:151], off offset:1792
	global_load_dword v126, v[150:151], off offset:1920

; __device__ __forceinline__ void p4_router(const Params& p, Frame& F) {
;     ...
;         if (F.tid < 32) hist[F.tid] = 0;
;         __syncthreads();
;         int es[4] = {0, 0, 0, 0}, lp[4] = {0, 0, 0, 0}; float gv[4] = {0.f, 0.f, 0.f, 0.f}; float rs = 0.f; const int t = blk * 64 + F.tid;
;         if (F.tid < 64) {
;             const int gg = F.tid >> 5, mm = F.tid & 31;
;             float s = 0.f;
; #pragma unroll
;             for (int q = 0; q < 4; ++q) s += ssqp[(gg * 4 + q) * 32 + mm];
;             rs = 1.0f / sqrtf(s * (1.0f / DM) + EPS);
;             float lg[32];
; #pragma unroll
;             for (int e = 0; e < 32; ++e) { float v = 0.f;
; #pragma unroll
;                 for (int q = 0; q < 4; ++q) v += part[((gg * 4 + q) * 32 + mm) * 32 + e];
;                 lg[e] = v * rs + p.in[13][e]; }
.LBB0_774:
	s_or_b64 exec, exec, s[6:7]
	s_and_saveexec_b64 s[6:7], s[2:3]
	ds_write_b32 v107, v83
	s_or_b64 exec, exec, s[6:7]
	v_mov_b32_e32 v50, 0
	v_mov_b32_e32 v7, 0
	v_mov_b32_e32 v8, 0
	v_mov_b32_e32 v9, 0
	v_mov_b32_e32 v10, 0
	v_mov_b32_e32 v6, 0
	v_mov_b32_e32 v36, 0
	v_mov_b32_e32 v19, 0
	s_waitcnt lgkmcnt(0)
	v_mov_b32_e32 v18, 0
	v_mov_b32_e32 v4, 0
	v_mov_b32_e32 v5, 0
	v_mov_b32_e32 v2, 0
	v_mov_b32_e32 v3, 0
	s_barrier
	s_and_saveexec_b64 s[30:31], s[4:5]
	s_cbranch_execz .LBB0_778
	v_add_u32_e32 v4, 0x8000, v108
	ds_read2_b32 v[2:3], v4 offset1:32
	v_readlane_b32 s68, v245, 39
	v_readlane_b32 s78, v245, 49
	v_readlane_b32 s79, v245, 50
	v_readlane_b32 s69, v245, 40
	s_waitcnt lgkmcnt(0)
	v_add_f32_e32 v2, 0, v2
	v_add_f32_e32 v5, v2, v3
	ds_read2_b32 v[2:3], v4 offset0:64 offset1:96
	ds_read_b128 v[30:33], v109
	ds_read_b128 v[26:29], v109 offset:16
	ds_read_b128 v[22:25], v109 offset:32
	ds_read_b128 v[18:21], v109 offset:48
	ds_read_b128 v[34:37], v109 offset:4096
	ds_read_b128 v[38:41], v109 offset:8192
	ds_read_b128 v[42:45], v109 offset:12288
	s_waitcnt lgkmcnt(7)
	v_add_f32_e32 v2, v5, v2
	v_add_f32_e32 v2, v2, v3
	v_fmamk_f32 v2, v2, 0x3a000000, v113
	v_cmp_gt_f32_e32 vcc, s41, v2
	v_mul_f32_e32 v3, 0x4f800000, v2
	v_readlane_b32 s70, v245, 41
	v_cndmask_b32_e32 v2, v2, v3, vcc
	v_sqrt_f32_e32 v3, v2
	v_readlane_b32 s71, v245, 42
	v_readlane_b32 s72, v245, 43
	v_readlane_b32 s73, v245, 44
	v_add_u32_e32 v4, -1, v3
	v_fma_f32 v5, -v4, v3, v2
	v_cmp_ge_f32_e64 s[6:7], 0, v5
	v_add_u32_e32 v5, 1, v3
	v_readlane_b32 s74, v245, 45
	v_cndmask_b32_e64 v4, v3, v4, s[6:7]
	v_fma_f32 v3, -v5, v3, v2
	v_cmp_lt_f32_e64 s[6:7], 0, v3
	v_readlane_b32 s75, v245, 46
	v_readlane_b32 s76, v245, 47
	v_cndmask_b32_e64 v3, v4, v5, s[6:7]
	v_mul_f32_e32 v4, 0x37800000, v3
	v_cndmask_b32_e32 v3, v3, v4, vcc
	v_cmp_class_f32_e32 vcc, v2, v115
	v_readlane_b32 s77, v245, 48
	v_readlane_b32 s80, v245, 51
	v_cndmask_b32_e32 v2, v3, v2, vcc
	v_div_scale_f32 v3, s[6:7], v2, v2, 1.0
	v_rcp_f32_e32 v4, v3
	v_readlane_b32 s81, v245, 52
	v_readlane_b32 s82, v245, 53
	v_readlane_b32 s83, v245, 54
	v_fma_f32 v5, -v3, v4, 1.0
	v_fmac_f32_e32 v4, v5, v4
	v_div_scale_f32 v5, vcc, 1.0, v2, 1.0
	v_mul_f32_e32 v6, v5, v4
	v_fma_f32 v7, -v3, v6, v5
	v_fmac_f32_e32 v6, v7, v4
	v_fma_f32 v3, -v3, v6, v5
	v_div_fmas_f32 v3, v3, v4, v6
	v_div_fixup_f32 v50, v3, v2, 1.0
	s_waitcnt lgkmcnt(6)
	v_add_f32_e32 v2, 0, v30
	s_waitcnt lgkmcnt(2)
	v_add_f32_e32 v2, v2, v34
	s_waitcnt lgkmcnt(1)
	v_add_f32_e32 v2, v2, v38
	s_waitcnt lgkmcnt(0)
	v_add_f32_e32 v30, v2, v42
	global_load_dwordx4 v[2:5], v83, s[78:79] offset:48 nt
	global_load_dwordx4 v[6:9], v83, s[78:79] offset:32 nt
	global_load_dwordx4 v[10:13], v83, s[78:79] offset:16 nt
	global_load_dwordx4 v[14:17], v83, s[78:79] nt
	ds_read_b128 v[46:49], v109 offset:12352
	s_waitcnt vmcnt(0)
	v_fma_f32 v51, v50, v30, v14
	v_add_f32_e32 v14, 0, v31
	v_add_f32_e32 v14, v14, v35
	v_add_f32_e32 v14, v14, v39
	v_add_f32_e32 v14, v14, v43
	v_fma_f32 v15, v50, v14, v15
	v_add_f32_e32 v14, 0, v32
	v_add_f32_e32 v14, v14, v36
	v_add_f32_e32 v14, v14, v40
	v_add_f32_e32 v14, v14, v44
	v_fma_f32 v14, v50, v14, v16
	v_add_f32_e32 v16, 0, v33
	ds_read_b128 v[30:33], v109 offset:4112
	v_add_f32_e32 v16, v16, v37
	ds_read_b128 v[34:37], v109 offset:8208
	v_add_f32_e32 v16, v16, v41
	ds_read_b128 v[38:41], v109 offset:12304
	v_add_f32_e32 v16, v16, v45
	v_fmac_f32_e32 v17, v50, v16
	v_add_f32_e32 v16, 0, v26
	s_waitcnt lgkmcnt(2)
	v_add_f32_e32 v16, v16, v30
	s_waitcnt lgkmcnt(1)
	v_add_f32_e32 v16, v16, v34
	s_waitcnt lgkmcnt(0)
	v_add_f32_e32 v16, v16, v38
	v_fma_f32 v16, v50, v16, v10
	v_add_f32_e32 v10, 0, v27
	v_add_f32_e32 v10, v10, v31
	v_add_f32_e32 v10, v10, v35
	v_add_f32_e32 v10, v10, v39
	v_fma_f32 v11, v50, v10, v11
	v_add_f32_e32 v10, 0, v28
	v_add_f32_e32 v10, v10, v32
	v_add_f32_e32 v10, v10, v36
	v_add_f32_e32 v10, v10, v40
	v_fma_f32 v10, v50, v10, v12
	v_add_f32_e32 v12, 0, v29
	ds_read_b128 v[26:29], v109 offset:4128
	v_add_f32_e32 v12, v12, v33
	ds_read_b128 v[30:33], v109 offset:8224
	ds_read_b128 v[42:45], v109 offset:8256
	v_add_f32_e32 v12, v12, v37
	ds_read_b128 v[34:37], v109 offset:12320
	v_add_f32_e32 v12, v12, v41
	v_fmac_f32_e32 v13, v50, v12
	v_add_f32_e32 v12, 0, v22
	ds_read_b128 v[38:41], v109 offset:4160
	s_waitcnt lgkmcnt(4)
	v_add_f32_e32 v12, v12, v26
	s_waitcnt lgkmcnt(3)
	v_add_f32_e32 v12, v12, v30
	s_waitcnt lgkmcnt(1)
	v_add_f32_e32 v12, v12, v34
	v_fma_f32 v12, v50, v12, v6
	v_add_f32_e32 v6, 0, v23
	v_add_f32_e32 v6, v6, v27
	v_add_f32_e32 v6, v6, v31
	v_add_f32_e32 v6, v6, v35
	v_fma_f32 v7, v50, v6, v7
	v_add_f32_e32 v6, 0, v24
	v_add_f32_e32 v6, v6, v28
	v_add_f32_e32 v6, v6, v32
	v_add_f32_e32 v6, v6, v36
	v_fma_f32 v6, v50, v6, v8
	v_add_f32_e32 v8, 0, v25
	ds_read_b128 v[22:25], v109 offset:4144
	v_add_f32_e32 v8, v8, v29
	ds_read_b128 v[26:29], v109 offset:8240
	v_add_f32_e32 v8, v8, v33
	ds_read_b128 v[30:33], v109 offset:12336
	v_add_f32_e32 v8, v8, v37
	v_fmac_f32_e32 v9, v50, v8
	v_add_f32_e32 v8, 0, v18
	ds_read_b128 v[34:37], v109 offset:64
	s_waitcnt lgkmcnt(3)
	v_add_f32_e32 v8, v8, v22
	s_waitcnt lgkmcnt(2)
	v_add_f32_e32 v8, v8, v26
	s_waitcnt lgkmcnt(1)
	v_add_f32_e32 v8, v8, v30
	v_fma_f32 v8, v50, v8, v2
	v_add_f32_e32 v2, 0, v19
	v_add_f32_e32 v2, v2, v23
	v_add_f32_e32 v2, v2, v27
	v_add_f32_e32 v2, v2, v31
	v_fma_f32 v3, v50, v2, v3
	v_add_f32_e32 v2, 0, v20
	v_add_f32_e32 v2, v2, v24
	v_add_f32_e32 v2, v2, v28
	v_add_f32_e32 v2, v2, v32
	v_fma_f32 v2, v50, v2, v4
	v_add_f32_e32 v4, 0, v21
	v_add_f32_e32 v4, v4, v25
	v_add_f32_e32 v4, v4, v29
	v_add_f32_e32 v4, v4, v33
	global_load_dwordx4 v[18:21], v83, s[78:79] offset:112 nt
	global_load_dwordx4 v[22:25], v83, s[78:79] offset:96 nt
	global_load_dwordx4 v[26:29], v83, s[78:79] offset:80 nt
	global_load_dwordx4 v[30:33], v83, s[78:79] offset:64 nt
	v_fmac_f32_e32 v5, v50, v4
	s_waitcnt lgkmcnt(0)
; __device__ __forceinline__ void p4_router(const Params& p, Frame& F) {
;     ...
;             for (int q = 0; q < 4; ++q) s += ssqp[(gg * 4 + q) * 32 + mm];
;             rs = 1.0f / sqrtf(s * (1.0f / DM) + EPS);
;             float lg[32];
; #pragma unroll
;             for (int e = 0; e < 32; ++e) { float v = 0.f;
; #pragma unroll
;                 for (int q = 0; q < 4; ++q) v += part[((gg * 4 + q) * 32 + mm) * 32 + e];
;                 lg[e] = v * rs + p.in[13][e]; }
;             unsigned used = 0u; float tv[4];
; #pragma unroll
;             for (int j = 0; j < 4; ++j) { float best = -3.0e38f; int bi = 0;
; #pragma unroll
;                 for (int e = 0; e < 32; ++e) { const bool ok = !((used >> e) & 1u) && (lg[e] > best); best = ok ? lg[e] : best; bi = ok ? e : bi; }
;                 used |= 1u << bi; es[j] = bi; tv[j] = best; }
	v_add_f32_e32 v4, 0, v34
	v_add_f32_e32 v4, v4, v38
	v_add_f32_e32 v4, v4, v42
	v_add_f32_e32 v4, v4, v46
	v_cmp_lt_f32_e32 vcc, s42, v51
	ds_read_b128 v[52:55], v109 offset:12368
	s_waitcnt vmcnt(0)
	v_fma_f32 v34, v50, v4, v30
	v_add_f32_e32 v4, 0, v35
	v_add_f32_e32 v4, v4, v39
	v_add_f32_e32 v4, v4, v43
	v_add_f32_e32 v4, v4, v47
	v_fma_f32 v30, v50, v4, v31
	v_add_f32_e32 v4, 0, v36
	v_add_f32_e32 v31, 0, v37
	ds_read_b128 v[36:39], v109 offset:80
	v_add_f32_e32 v4, v4, v40
	v_add_f32_e32 v31, v31, v41
	ds_read_b128 v[40:43], v109 offset:4176
	v_add_f32_e32 v4, v4, v44
	v_add_f32_e32 v31, v31, v45
	ds_read_b128 v[44:47], v109 offset:8272
	v_add_f32_e32 v31, v31, v49
	v_fmac_f32_e32 v33, v50, v31
	s_waitcnt lgkmcnt(2)
	v_add_f32_e32 v31, 0, v36
	s_waitcnt lgkmcnt(1)
	v_add_f32_e32 v31, v31, v40
	s_waitcnt lgkmcnt(0)
	v_add_f32_e32 v31, v31, v44
	v_add_f32_e32 v31, v31, v52
	v_fma_f32 v31, v50, v31, v26
	v_add_f32_e32 v26, 0, v37
	v_add_f32_e32 v26, v26, v41
	v_add_f32_e32 v26, v26, v45
	v_add_f32_e32 v26, v26, v53
	v_fma_f32 v27, v50, v26, v27
	v_add_f32_e32 v26, 0, v38
	v_add_f32_e32 v26, v26, v42
	v_add_f32_e32 v26, v26, v46
	v_add_f32_e32 v26, v26, v54
	v_fma_f32 v26, v50, v26, v28
	v_add_f32_e32 v28, 0, v39
	ds_read_b128 v[36:39], v109 offset:96
	v_add_f32_e32 v28, v28, v43
	ds_read_b128 v[40:43], v109 offset:4192
	v_add_f32_e32 v28, v28, v47
	ds_read_b128 v[44:47], v109 offset:8288
	v_add_f32_e32 v28, v28, v55
	ds_read_b128 v[52:55], v109 offset:12384
	v_fmac_f32_e32 v29, v50, v28
	s_waitcnt lgkmcnt(3)
	v_add_f32_e32 v28, 0, v36
	s_waitcnt lgkmcnt(2)
	v_add_f32_e32 v28, v28, v40
	s_waitcnt lgkmcnt(1)
	v_add_f32_e32 v28, v28, v44
	s_waitcnt lgkmcnt(0)
	v_add_f32_e32 v28, v28, v52
	v_fma_f32 v28, v50, v28, v22
	v_add_f32_e32 v22, 0, v37
	v_add_f32_e32 v22, v22, v41
	v_add_f32_e32 v22, v22, v45
	v_add_f32_e32 v22, v22, v53
	v_fma_f32 v23, v50, v22, v23
	v_add_f32_e32 v22, 0, v38
	v_add_f32_e32 v22, v22, v42
	v_add_f32_e32 v22, v22, v46
	v_add_f32_e32 v22, v22, v54
	v_fma_f32 v22, v50, v22, v24
	v_add_f32_e32 v24, 0, v39
	ds_read_b128 v[36:39], v109 offset:112
	v_add_f32_e32 v24, v24, v43
	ds_read_b128 v[40:43], v109 offset:4208
	v_add_f32_e32 v24, v24, v47
	ds_read_b128 v[44:47], v109 offset:8304
	v_add_f32_e32 v24, v24, v55
	ds_read_b128 v[52:55], v109 offset:12400
	v_fmac_f32_e32 v25, v50, v24
	s_waitcnt lgkmcnt(3)
	v_add_f32_e32 v24, 0, v36
	s_waitcnt lgkmcnt(2)
	v_add_f32_e32 v24, v24, v40
	s_waitcnt lgkmcnt(1)
	v_add_f32_e32 v24, v24, v44
	v_add_f32_e32 v4, v4, v48
	s_waitcnt lgkmcnt(0)
	v_add_f32_e32 v24, v24, v52
	v_fma_f32 v4, v50, v4, v32
	v_fma_f32 v32, v50, v24, v18
	v_add_f32_e32 v18, 0, v37
	v_add_f32_e32 v18, v18, v41
	v_add_f32_e32 v18, v18, v45
	v_add_f32_e32 v18, v18, v53
	v_fma_f32 v24, v50, v18, v19
	v_add_f32_e32 v18, 0, v38
	v_add_f32_e32 v18, v18, v42
	v_add_f32_e32 v18, v18, v46
	v_add_f32_e32 v18, v18, v54
	v_fma_f32 v20, v50, v18, v20
	v_add_f32_e32 v18, 0, v39
	v_add_f32_e32 v18, v18, v43
	v_add_f32_e32 v18, v18, v47
	v_add_f32_e32 v18, v18, v55
	v_fmac_f32_e32 v21, v50, v18
	v_max_f32_e32 v18, v51, v51
	v_max_f32_e32 v18, 0xff61b1e6, v18
	v_cmp_gt_f32_e64 s[6:7], v15, v18
	s_nop 1
	v_cndmask_b32_e64 v18, v18, v15, s[6:7]
	v_cndmask_b32_e64 v19, 0, 1, s[6:7]
	v_cmp_gt_f32_e64 s[6:7], v14, v18
	s_nop 1
	v_cndmask_b32_e64 v18, v18, v14, s[6:7]
	v_cndmask_b32_e64 v19, v19, 2, s[6:7]
	v_cmp_gt_f32_e64 s[6:7], v17, v18
	s_nop 1
	v_cndmask_b32_e64 v18, v18, v17, s[6:7]
	v_cndmask_b32_e64 v19, v19, 3, s[6:7]
	v_cmp_gt_f32_e64 s[6:7], v16, v18
	s_nop 1
	v_cndmask_b32_e64 v18, v18, v16, s[6:7]
	v_cndmask_b32_e64 v19, v19, 4, s[6:7]
	v_cmp_gt_f32_e64 s[6:7], v11, v18
	s_nop 1
	v_cndmask_b32_e64 v18, v18, v11, s[6:7]
	v_cndmask_b32_e64 v19, v19, 5, s[6:7]
	v_cmp_gt_f32_e64 s[6:7], v10, v18
	s_nop 1
	v_cndmask_b32_e64 v18, v18, v10, s[6:7]
	v_cndmask_b32_e64 v19, v19, 6, s[6:7]
	v_cmp_gt_f32_e64 s[6:7], v13, v18
	s_nop 1
	v_cndmask_b32_e64 v18, v18, v13, s[6:7]
	v_cndmask_b32_e64 v19, v19, 7, s[6:7]
	v_cmp_gt_f32_e64 s[6:7], v12, v18
	s_nop 1
	v_cndmask_b32_e64 v18, v18, v12, s[6:7]
	v_cndmask_b32_e64 v19, v19, 8, s[6:7]
	v_cmp_gt_f32_e64 s[6:7], v7, v18
	s_nop 1
	v_cndmask_b32_e64 v18, v18, v7, s[6:7]
	v_cndmask_b32_e64 v19, v19, 9, s[6:7]
	v_cmp_gt_f32_e64 s[6:7], v6, v18
	s_nop 1
	v_cndmask_b32_e64 v18, v18, v6, s[6:7]
	v_cndmask_b32_e64 v19, v19, 10, s[6:7]
	v_cmp_gt_f32_e64 s[6:7], v9, v18
	s_nop 1
	v_cndmask_b32_e64 v18, v18, v9, s[6:7]
	v_cndmask_b32_e64 v19, v19, 11, s[6:7]
	v_cmp_gt_f32_e64 s[6:7], v8, v18
	s_nop 1
	v_cndmask_b32_e64 v18, v18, v8, s[6:7]
	v_cndmask_b32_e64 v19, v19, 12, s[6:7]
	v_cmp_gt_f32_e64 s[6:7], v3, v18
	s_nop 1
	v_cndmask_b32_e64 v18, v18, v3, s[6:7]
	v_cndmask_b32_e64 v19, v19, 13, s[6:7]
	v_cmp_gt_f32_e64 s[6:7], v2, v18
	s_nop 1
	v_cndmask_b32_e64 v18, v18, v2, s[6:7]
	v_cndmask_b32_e64 v19, v19, 14, s[6:7]
	v_cmp_gt_f32_e64 s[6:7], v5, v18
	s_nop 1
	v_cndmask_b32_e64 v18, v18, v5, s[6:7]
	v_cndmask_b32_e64 v19, v19, 15, s[6:7]
	v_cmp_gt_f32_e64 s[6:7], v34, v18
	s_nop 1
	v_cndmask_b32_e64 v18, v18, v34, s[6:7]
	v_cndmask_b32_e64 v19, v19, 16, s[6:7]
	v_cmp_gt_f32_e64 s[6:7], v30, v18
	s_nop 1
	v_cndmask_b32_e64 v18, v18, v30, s[6:7]
	v_cndmask_b32_e64 v19, v19, 17, s[6:7]
	v_cmp_gt_f32_e64 s[6:7], v4, v18
	s_nop 1
	v_cndmask_b32_e64 v18, v18, v4, s[6:7]
	v_cndmask_b32_e64 v19, v19, 18, s[6:7]
	v_cmp_gt_f32_e64 s[6:7], v33, v18
	s_nop 1
	v_cndmask_b32_e64 v18, v18, v33, s[6:7]
	v_cndmask_b32_e64 v19, v19, 19, s[6:7]
	v_cmp_gt_f32_e64 s[6:7], v31, v18
	s_nop 1
	v_cndmask_b32_e64 v18, v18, v31, s[6:7]
	v_cndmask_b32_e64 v19, v19, 20, s[6:7]
	v_cmp_gt_f32_e64 s[6:7], v27, v18
; __device__ __forceinline__ void p4_router(const Params& p, Frame& F) {
;     ...
;             unsigned used = 0u; float tv[4];
; #pragma unroll
;             for (int j = 0; j < 4; ++j) { float best = -3.0e38f; int bi = 0;
; #pragma unroll
;                 for (int e = 0; e < 32; ++e) { const bool ok = !((used >> e) & 1u) && (lg[e] > best); best = ok ? lg[e] : best; bi = ok ? e : bi; }
;                 used |= 1u << bi; es[j] = bi; tv[j] = best; }
	s_nop 1
	v_cndmask_b32_e64 v18, v18, v27, s[6:7]
	v_cndmask_b32_e64 v19, v19, 21, s[6:7]
	v_cmp_gt_f32_e64 s[6:7], v26, v18
	s_nop 1
	v_cndmask_b32_e64 v18, v18, v26, s[6:7]
	v_cndmask_b32_e64 v19, v19, 22, s[6:7]
	v_cmp_gt_f32_e64 s[6:7], v29, v18
	s_nop 1
	v_cndmask_b32_e64 v18, v18, v29, s[6:7]
	v_cndmask_b32_e64 v19, v19, 23, s[6:7]
	v_cmp_gt_f32_e64 s[6:7], v28, v18
	s_nop 1
	v_cndmask_b32_e64 v18, v18, v28, s[6:7]
	v_cndmask_b32_e64 v19, v19, 24, s[6:7]
	v_cmp_gt_f32_e64 s[6:7], v23, v18
	s_nop 1
	v_cndmask_b32_e64 v18, v18, v23, s[6:7]
	v_cndmask_b32_e64 v19, v19, 25, s[6:7]
	v_cmp_gt_f32_e64 s[6:7], v22, v18
	s_nop 1
	v_cndmask_b32_e64 v18, v18, v22, s[6:7]
	v_cndmask_b32_e64 v19, v19, 26, s[6:7]
	v_cmp_gt_f32_e64 s[6:7], v25, v18
	s_nop 1
	v_cndmask_b32_e64 v18, v18, v25, s[6:7]
	v_cndmask_b32_e64 v19, v19, 27, s[6:7]
	v_cmp_gt_f32_e64 s[6:7], v32, v18
	s_nop 1
	v_cndmask_b32_e64 v18, v18, v32, s[6:7]
	v_cndmask_b32_e64 v19, v19, 28, s[6:7]
	v_cmp_gt_f32_e64 s[6:7], v24, v18
	s_nop 1
	v_cndmask_b32_e64 v18, v18, v24, s[6:7]
	v_cndmask_b32_e64 v19, v19, 29, s[6:7]
	v_cmp_gt_f32_e64 s[6:7], v20, v18
	s_nop 1
	v_cndmask_b32_e64 v35, v18, v20, s[6:7]
	v_cndmask_b32_e64 v19, v19, 30, s[6:7]
	v_cmp_gt_f32_e64 s[6:7], v21, v35
	s_nop 1
	v_cndmask_b32_e64 v18, v19, 31, s[6:7]
	v_cndmask_b32_e64 v35, v35, v21, s[6:7]
	v_cmp_ne_u32_e64 s[6:7], 0, v18
	v_lshlrev_b32_e64 v36, v18, 1
	s_and_b64 s[6:7], s[6:7], vcc
	v_cndmask_b32_e64 v19, v116, v51, s[6:7]
	v_and_b32_e32 v37, 2, v36
	v_cmp_eq_u32_e64 s[6:7], 0, v37
	v_cmp_gt_f32_e64 s[8:9], v15, v19
	s_and_b64 s[6:7], s[6:7], s[8:9]
	v_cndmask_b32_e64 v19, v19, v15, s[6:7]
	v_and_b32_e32 v38, 4, v36
	v_cndmask_b32_e64 v37, 0, 1, s[6:7]
	v_cmp_eq_u32_e64 s[6:7], 0, v38
	v_cmp_gt_f32_e64 s[8:9], v14, v19
	s_and_b64 s[6:7], s[6:7], s[8:9]
	v_cndmask_b32_e64 v19, v19, v14, s[6:7]
	v_and_b32_e32 v38, 8, v36
	v_cndmask_b32_e64 v37, v37, 2, s[6:7]
	v_cmp_eq_u32_e64 s[6:7], 0, v38
	v_cmp_gt_f32_e64 s[8:9], v17, v19
	s_and_b64 s[6:7], s[6:7], s[8:9]
	v_cndmask_b32_e64 v19, v19, v17, s[6:7]
	v_and_b32_e32 v38, 16, v36
	v_cndmask_b32_e64 v37, v37, 3, s[6:7]
	v_cmp_eq_u32_e64 s[6:7], 0, v38
	v_cmp_gt_f32_e64 s[8:9], v16, v19
	s_and_b64 s[6:7], s[6:7], s[8:9]
	v_cndmask_b32_e64 v19, v19, v16, s[6:7]
	v_and_b32_e32 v38, 32, v36
	v_cndmask_b32_e64 v37, v37, 4, s[6:7]
	v_cmp_eq_u32_e64 s[6:7], 0, v38
	v_cmp_gt_f32_e64 s[8:9], v11, v19
	s_and_b64 s[6:7], s[6:7], s[8:9]
	v_cndmask_b32_e64 v19, v19, v11, s[6:7]
	v_and_b32_e32 v38, 64, v36
	v_cndmask_b32_e64 v37, v37, 5, s[6:7]
	v_cmp_eq_u32_e64 s[6:7], 0, v38
	v_cmp_gt_f32_e64 s[8:9], v10, v19
	s_and_b64 s[6:7], s[6:7], s[8:9]
	v_cndmask_b32_e64 v19, v19, v10, s[6:7]
	v_and_b32_e32 v38, 0x80, v36
	v_cndmask_b32_e64 v37, v37, 6, s[6:7]
	v_cmp_eq_u32_e64 s[6:7], 0, v38
	v_cmp_gt_f32_e64 s[8:9], v13, v19
	s_and_b64 s[6:7], s[6:7], s[8:9]
	v_cndmask_b32_e64 v19, v19, v13, s[6:7]
	v_and_b32_e32 v38, 0x100, v36
	v_cndmask_b32_e64 v37, v37, 7, s[6:7]
	v_cmp_eq_u32_e64 s[6:7], 0, v38
	v_cmp_gt_f32_e64 s[8:9], v12, v19
	s_and_b64 s[6:7], s[6:7], s[8:9]
	v_cndmask_b32_e64 v19, v19, v12, s[6:7]
	v_and_b32_e32 v38, 0x200, v36
	v_cndmask_b32_e64 v37, v37, 8, s[6:7]
	v_cmp_eq_u32_e64 s[6:7], 0, v38
	v_cmp_gt_f32_e64 s[8:9], v7, v19
	s_and_b64 s[6:7], s[6:7], s[8:9]
	v_cndmask_b32_e64 v19, v19, v7, s[6:7]
	v_and_b32_e32 v38, 0x400, v36
	v_cndmask_b32_e64 v37, v37, 9, s[6:7]
	v_cmp_eq_u32_e64 s[6:7], 0, v38
	v_cmp_gt_f32_e64 s[8:9], v6, v19
	s_and_b64 s[6:7], s[6:7], s[8:9]
	v_cndmask_b32_e64 v19, v19, v6, s[6:7]
	v_and_b32_e32 v38, 0x800, v36
	v_cndmask_b32_e64 v37, v37, 10, s[6:7]
	v_cmp_eq_u32_e64 s[6:7], 0, v38
	v_cmp_gt_f32_e64 s[8:9], v9, v19
	s_and_b64 s[6:7], s[6:7], s[8:9]
	v_cndmask_b32_e64 v19, v19, v9, s[6:7]
	v_and_b32_e32 v38, 0x1000, v36
	v_cndmask_b32_e64 v37, v37, 11, s[6:7]
	v_cmp_eq_u32_e64 s[6:7], 0, v38
	v_cmp_gt_f32_e64 s[8:9], v8, v19
	s_and_b64 s[6:7], s[6:7], s[8:9]
	v_cndmask_b32_e64 v19, v19, v8, s[6:7]
	v_and_b32_e32 v38, 0x2000, v36
	v_cndmask_b32_e64 v37, v37, 12, s[6:7]
	v_cmp_eq_u32_e64 s[6:7], 0, v38
	v_cmp_gt_f32_e64 s[8:9], v3, v19
	s_and_b64 s[6:7], s[6:7], s[8:9]
	v_cndmask_b32_e64 v19, v19, v3, s[6:7]
	v_and_b32_e32 v38, 0x4000, v36
	v_cndmask_b32_e64 v37, v37, 13, s[6:7]
	v_cmp_eq_u32_e64 s[6:7], 0, v38
	v_cmp_gt_f32_e64 s[8:9], v2, v19
	s_and_b64 s[6:7], s[6:7], s[8:9]
	v_cndmask_b32_e64 v19, v19, v2, s[6:7]
	v_and_b32_e32 v38, 0x8000, v36
	v_cndmask_b32_e64 v37, v37, 14, s[6:7]
	v_cmp_eq_u32_e64 s[6:7], 0, v38
	v_cmp_gt_f32_e64 s[8:9], v5, v19
	s_and_b64 s[6:7], s[6:7], s[8:9]
	v_cndmask_b32_e64 v19, v19, v5, s[6:7]
	v_and_b32_e32 v38, 0x10000, v36
	v_cndmask_b32_e64 v37, v37, 15, s[6:7]
	v_cmp_eq_u32_e64 s[6:7], 0, v38
	v_cmp_gt_f32_e64 s[8:9], v34, v19
	s_and_b64 s[6:7], s[6:7], s[8:9]
	v_cndmask_b32_e64 v19, v19, v34, s[6:7]
	v_and_b32_e32 v38, 0x20000, v36
	v_cndmask_b32_e64 v37, v37, 16, s[6:7]
	v_cmp_eq_u32_e64 s[6:7], 0, v38
	v_cmp_gt_f32_e64 s[8:9], v30, v19
	s_and_b64 s[6:7], s[6:7], s[8:9]
	v_cndmask_b32_e64 v19, v19, v30, s[6:7]
	v_and_b32_e32 v38, 0x40000, v36
	v_cndmask_b32_e64 v37, v37, 17, s[6:7]
	v_cmp_eq_u32_e64 s[6:7], 0, v38
	v_cmp_gt_f32_e64 s[8:9], v4, v19
	s_and_b64 s[6:7], s[6:7], s[8:9]
	v_cndmask_b32_e64 v19, v19, v4, s[6:7]
	v_and_b32_e32 v38, 0x80000, v36
	v_cndmask_b32_e64 v37, v37, 18, s[6:7]
	v_cmp_eq_u32_e64 s[6:7], 0, v38
	v_cmp_gt_f32_e64 s[8:9], v33, v19
	s_and_b64 s[6:7], s[6:7], s[8:9]
	v_cndmask_b32_e64 v19, v19, v33, s[6:7]
	v_and_b32_e32 v38, 0x100000, v36
	v_cndmask_b32_e64 v37, v37, 19, s[6:7]
	v_cmp_eq_u32_e64 s[6:7], 0, v38
	v_cmp_gt_f32_e64 s[8:9], v31, v19
	s_and_b64 s[6:7], s[6:7], s[8:9]
; __device__ __forceinline__ void p4_router(const Params& p, Frame& F) {
;     ...
;             unsigned used = 0u; float tv[4];
; #pragma unroll
;             for (int j = 0; j < 4; ++j) { float best = -3.0e38f; int bi = 0;
; #pragma unroll
;                 for (int e = 0; e < 32; ++e) { const bool ok = !((used >> e) & 1u) && (lg[e] > best); best = ok ? lg[e] : best; bi = ok ? e : bi; }
;                 used |= 1u << bi; es[j] = bi; tv[j] = best; }
	v_cndmask_b32_e64 v19, v19, v31, s[6:7]
	v_and_b32_e32 v38, 0x200000, v36
	v_cndmask_b32_e64 v37, v37, 20, s[6:7]
	v_cmp_eq_u32_e64 s[6:7], 0, v38
	v_cmp_gt_f32_e64 s[8:9], v27, v19
	s_and_b64 s[6:7], s[6:7], s[8:9]
	v_cndmask_b32_e64 v19, v19, v27, s[6:7]
	v_and_b32_e32 v38, 0x400000, v36
	v_cndmask_b32_e64 v37, v37, 21, s[6:7]
	v_cmp_eq_u32_e64 s[6:7], 0, v38
	v_cmp_gt_f32_e64 s[8:9], v26, v19
	s_and_b64 s[6:7], s[6:7], s[8:9]
	v_cndmask_b32_e64 v19, v19, v26, s[6:7]
	v_and_b32_e32 v38, 0x800000, v36
	v_cndmask_b32_e64 v37, v37, 22, s[6:7]
	v_cmp_eq_u32_e64 s[6:7], 0, v38
	v_cmp_gt_f32_e64 s[8:9], v29, v19
	s_and_b64 s[6:7], s[6:7], s[8:9]
	v_cndmask_b32_e64 v19, v19, v29, s[6:7]
	v_and_b32_e32 v38, 0x1000000, v36
	v_cndmask_b32_e64 v37, v37, 23, s[6:7]
	v_cmp_eq_u32_e64 s[6:7], 0, v38
	v_cmp_gt_f32_e64 s[8:9], v28, v19
	s_and_b64 s[6:7], s[6:7], s[8:9]
	v_cndmask_b32_e64 v19, v19, v28, s[6:7]
	v_and_b32_e32 v38, 0x2000000, v36
	v_cndmask_b32_e64 v37, v37, 24, s[6:7]
	v_cmp_eq_u32_e64 s[6:7], 0, v38
	v_cmp_gt_f32_e64 s[8:9], v23, v19
	s_and_b64 s[6:7], s[6:7], s[8:9]
	v_cndmask_b32_e64 v19, v19, v23, s[6:7]
	v_and_b32_e32 v38, 0x4000000, v36
	v_cndmask_b32_e64 v37, v37, 25, s[6:7]
	v_cmp_eq_u32_e64 s[6:7], 0, v38
	v_cmp_gt_f32_e64 s[8:9], v22, v19
	s_and_b64 s[6:7], s[6:7], s[8:9]
	v_cndmask_b32_e64 v19, v19, v22, s[6:7]
	v_and_b32_e32 v38, 0x8000000, v36
	v_cndmask_b32_e64 v37, v37, 26, s[6:7]
	v_cmp_eq_u32_e64 s[6:7], 0, v38
	v_cmp_gt_f32_e64 s[8:9], v25, v19
	s_and_b64 s[6:7], s[6:7], s[8:9]
	v_cndmask_b32_e64 v19, v19, v25, s[6:7]
	v_and_b32_e32 v38, 0x10000000, v36
	v_cndmask_b32_e64 v37, v37, 27, s[6:7]
	v_cmp_eq_u32_e64 s[6:7], 0, v38
	v_cmp_gt_f32_e64 s[8:9], v32, v19
	s_and_b64 s[6:7], s[6:7], s[8:9]
	v_cndmask_b32_e64 v19, v19, v32, s[6:7]
	v_and_b32_e32 v38, 0x20000000, v36
	v_cndmask_b32_e64 v37, v37, 28, s[6:7]
	v_cmp_eq_u32_e64 s[6:7], 0, v38
	v_cmp_gt_f32_e64 s[8:9], v24, v19
	s_and_b64 s[6:7], s[6:7], s[8:9]
	v_cndmask_b32_e64 v19, v19, v24, s[6:7]
	v_and_b32_e32 v38, 2.0, v36
	v_cndmask_b32_e64 v37, v37, 29, s[6:7]
	v_cmp_eq_u32_e64 s[6:7], 0, v38
	v_cmp_gt_f32_e64 s[8:9], v20, v19
	s_and_b64 s[6:7], s[6:7], s[8:9]
	v_cndmask_b32_e64 v38, v19, v20, s[6:7]
	v_cndmask_b32_e64 v37, v37, 30, s[6:7]
	v_cmp_ne_u32_e64 s[6:7], 31, v18
	v_cmp_gt_f32_e64 s[8:9], v21, v38
	s_and_b64 s[6:7], s[6:7], s[8:9]
	v_cndmask_b32_e64 v19, v37, 31, s[6:7]
	v_cndmask_b32_e64 v37, v38, v21, s[6:7]
	v_lshlrev_b32_e64 v38, v19, 1
	v_bitop3_b32 v40, v38, 1, v36 bitop3:0xc8
	v_cmp_eq_u32_e64 s[6:7], 0, v40
	s_and_b64 s[6:7], s[6:7], vcc
	v_bitop3_b32 v41, v38, 2, v36 bitop3:0xc8
	v_cndmask_b32_e64 v40, v116, v51, s[6:7]
	v_cmp_eq_u32_e64 s[6:7], 0, v41
	v_cmp_gt_f32_e64 s[8:9], v15, v40
	s_and_b64 s[6:7], s[6:7], s[8:9]
	v_cndmask_b32_e64 v40, v40, v15, s[6:7]
	v_bitop3_b32 v42, v38, 4, v36 bitop3:0xc8
	v_cndmask_b32_e64 v41, 0, 1, s[6:7]
	v_cmp_eq_u32_e64 s[6:7], 0, v42
	v_cmp_gt_f32_e64 s[8:9], v14, v40
	s_and_b64 s[6:7], s[6:7], s[8:9]
	v_cndmask_b32_e64 v40, v40, v14, s[6:7]
	v_bitop3_b32 v42, v38, 8, v36 bitop3:0xc8
	v_cndmask_b32_e64 v41, v41, 2, s[6:7]
	v_cmp_eq_u32_e64 s[6:7], 0, v42
	v_cmp_gt_f32_e64 s[8:9], v17, v40
	s_and_b64 s[6:7], s[6:7], s[8:9]
	v_cndmask_b32_e64 v40, v40, v17, s[6:7]
	v_bitop3_b32 v42, v38, 16, v36 bitop3:0xc8
	v_cndmask_b32_e64 v41, v41, 3, s[6:7]
	v_cmp_eq_u32_e64 s[6:7], 0, v42
	v_cmp_gt_f32_e64 s[8:9], v16, v40
	s_and_b64 s[6:7], s[6:7], s[8:9]
	v_cndmask_b32_e64 v40, v40, v16, s[6:7]
	v_bitop3_b32 v42, v38, 32, v36 bitop3:0xc8
	v_cndmask_b32_e64 v41, v41, 4, s[6:7]
	v_cmp_eq_u32_e64 s[6:7], 0, v42
	v_cmp_gt_f32_e64 s[8:9], v11, v40
	s_and_b64 s[6:7], s[6:7], s[8:9]
	v_cndmask_b32_e64 v40, v40, v11, s[6:7]
	v_bitop3_b32 v42, v38, 64, v36 bitop3:0xc8
	v_cndmask_b32_e64 v41, v41, 5, s[6:7]
	v_cmp_eq_u32_e64 s[6:7], 0, v42
	v_cmp_gt_f32_e64 s[8:9], v10, v40
	s_and_b64 s[6:7], s[6:7], s[8:9]
	v_cndmask_b32_e64 v40, v40, v10, s[6:7]
	v_bitop3_b32 v42, v38, s43, v36 bitop3:0xc8
	v_cndmask_b32_e64 v41, v41, 6, s[6:7]
	v_cmp_eq_u32_e64 s[6:7], 0, v42
	v_cmp_gt_f32_e64 s[8:9], v13, v40
	s_and_b64 s[6:7], s[6:7], s[8:9]
	v_cndmask_b32_e64 v40, v40, v13, s[6:7]
	v_bitop3_b32 v42, v38, s44, v36 bitop3:0xc8
	v_cndmask_b32_e64 v41, v41, 7, s[6:7]
	v_cmp_eq_u32_e64 s[6:7], 0, v42
	v_cmp_gt_f32_e64 s[8:9], v12, v40
	s_and_b64 s[6:7], s[6:7], s[8:9]
	v_cndmask_b32_e64 v40, v40, v12, s[6:7]
	v_bitop3_b32 v42, v38, s35, v36 bitop3:0xc8
	v_cndmask_b32_e64 v41, v41, 8, s[6:7]
	v_cmp_eq_u32_e64 s[6:7], 0, v42
	v_cmp_gt_f32_e64 s[8:9], v7, v40
	s_and_b64 s[6:7], s[6:7], s[8:9]
	v_cndmask_b32_e64 v40, v40, v7, s[6:7]
	v_bitop3_b32 v42, v38, s45, v36 bitop3:0xc8
	v_cndmask_b32_e64 v41, v41, 9, s[6:7]
	v_cmp_eq_u32_e64 s[6:7], 0, v42
	v_cmp_gt_f32_e64 s[8:9], v6, v40
	s_and_b64 s[6:7], s[6:7], s[8:9]
	v_cndmask_b32_e64 v40, v40, v6, s[6:7]
	v_bitop3_b32 v42, v38, s46, v36 bitop3:0xc8
	v_cndmask_b32_e64 v41, v41, 10, s[6:7]
	v_cmp_eq_u32_e64 s[6:7], 0, v42
	v_cmp_gt_f32_e64 s[8:9], v9, v40
	s_and_b64 s[6:7], s[6:7], s[8:9]
	v_cndmask_b32_e64 v40, v40, v9, s[6:7]
	v_bitop3_b32 v42, v38, s40, v36 bitop3:0xc8
	v_cndmask_b32_e64 v41, v41, 11, s[6:7]
	v_cmp_eq_u32_e64 s[6:7], 0, v42
	v_cmp_gt_f32_e64 s[8:9], v8, v40
	s_and_b64 s[6:7], s[6:7], s[8:9]
	v_cndmask_b32_e64 v40, v40, v8, s[6:7]
	v_bitop3_b32 v42, v38, s47, v36 bitop3:0xc8
	v_cndmask_b32_e64 v41, v41, 12, s[6:7]
	v_cmp_eq_u32_e64 s[6:7], 0, v42
	v_cmp_gt_f32_e64 s[8:9], v3, v40
	s_and_b64 s[6:7], s[6:7], s[8:9]
	v_cndmask_b32_e64 v40, v40, v3, s[6:7]
	v_bitop3_b32 v42, v38, s48, v36 bitop3:0xc8
	v_cndmask_b32_e64 v41, v41, 13, s[6:7]
	v_cmp_eq_u32_e64 s[6:7], 0, v42
; __device__ __forceinline__ void p4_router(const Params& p, Frame& F) {
;     ...
;             unsigned used = 0u; float tv[4];
; #pragma unroll
;             for (int j = 0; j < 4; ++j) { float best = -3.0e38f; int bi = 0;
; #pragma unroll
;                 for (int e = 0; e < 32; ++e) { const bool ok = !((used >> e) & 1u) && (lg[e] > best); best = ok ? lg[e] : best; bi = ok ? e : bi; }
;                 used |= 1u << bi; es[j] = bi; tv[j] = best; }
	v_cmp_gt_f32_e64 s[8:9], v2, v40
	s_and_b64 s[6:7], s[6:7], s[8:9]
	v_cndmask_b32_e64 v40, v40, v2, s[6:7]
	v_bitop3_b32 v42, v38, s49, v36 bitop3:0xc8
	v_cndmask_b32_e64 v41, v41, 14, s[6:7]
	v_cmp_eq_u32_e64 s[6:7], 0, v42
	v_cmp_gt_f32_e64 s[8:9], v5, v40
	s_and_b64 s[6:7], s[6:7], s[8:9]
	v_cndmask_b32_e64 v40, v40, v5, s[6:7]
	v_bitop3_b32 v42, v38, s50, v36 bitop3:0xc8
	v_cndmask_b32_e64 v41, v41, 15, s[6:7]
	v_cmp_eq_u32_e64 s[6:7], 0, v42
	v_cmp_gt_f32_e64 s[8:9], v34, v40
	s_and_b64 s[6:7], s[6:7], s[8:9]
	v_cndmask_b32_e64 v40, v40, v34, s[6:7]
	v_bitop3_b32 v42, v38, s51, v36 bitop3:0xc8
	v_cndmask_b32_e64 v41, v41, 16, s[6:7]
	v_cmp_eq_u32_e64 s[6:7], 0, v42
	v_cmp_gt_f32_e64 s[8:9], v30, v40
	s_and_b64 s[6:7], s[6:7], s[8:9]
	v_cndmask_b32_e64 v40, v40, v30, s[6:7]
	v_bitop3_b32 v42, v38, s52, v36 bitop3:0xc8
	v_cndmask_b32_e64 v41, v41, 17, s[6:7]
	v_cmp_eq_u32_e64 s[6:7], 0, v42
	v_cmp_gt_f32_e64 s[8:9], v4, v40
	s_and_b64 s[6:7], s[6:7], s[8:9]
	v_cndmask_b32_e64 v40, v40, v4, s[6:7]
	v_bitop3_b32 v42, v38, s53, v36 bitop3:0xc8
	v_cndmask_b32_e64 v41, v41, 18, s[6:7]
	v_cmp_eq_u32_e64 s[6:7], 0, v42
	v_cmp_gt_f32_e64 s[8:9], v33, v40
	s_and_b64 s[6:7], s[6:7], s[8:9]
	v_cndmask_b32_e64 v40, v40, v33, s[6:7]
	v_bitop3_b32 v42, v38, s56, v36 bitop3:0xc8
	v_cndmask_b32_e64 v41, v41, 19, s[6:7]
	v_cmp_eq_u32_e64 s[6:7], 0, v42
	v_cmp_gt_f32_e64 s[8:9], v31, v40
	s_and_b64 s[6:7], s[6:7], s[8:9]
	v_cndmask_b32_e64 v40, v40, v31, s[6:7]
	v_bitop3_b32 v42, v38, s57, v36 bitop3:0xc8
	v_cndmask_b32_e64 v41, v41, 20, s[6:7]
	v_cmp_eq_u32_e64 s[6:7], 0, v42
	v_cmp_gt_f32_e64 s[8:9], v27, v40
	s_and_b64 s[6:7], s[6:7], s[8:9]
	v_cndmask_b32_e64 v40, v40, v27, s[6:7]
	v_bitop3_b32 v42, v38, s58, v36 bitop3:0xc8
	v_cndmask_b32_e64 v41, v41, 21, s[6:7]
	v_cmp_eq_u32_e64 s[6:7], 0, v42
	v_cmp_gt_f32_e64 s[8:9], v26, v40
	s_and_b64 s[6:7], s[6:7], s[8:9]
	v_cndmask_b32_e64 v40, v40, v26, s[6:7]
	v_bitop3_b32 v42, v38, s59, v36 bitop3:0xc8
	v_cndmask_b32_e64 v41, v41, 22, s[6:7]
	v_cmp_eq_u32_e64 s[6:7], 0, v42
	v_cmp_gt_f32_e64 s[8:9], v29, v40
	s_and_b64 s[6:7], s[6:7], s[8:9]
	v_cndmask_b32_e64 v40, v40, v29, s[6:7]
	v_bitop3_b32 v42, v38, s60, v36 bitop3:0xc8
	v_cndmask_b32_e64 v41, v41, 23, s[6:7]
	v_cmp_eq_u32_e64 s[6:7], 0, v42
	v_cmp_gt_f32_e64 s[8:9], v28, v40
	s_and_b64 s[6:7], s[6:7], s[8:9]
	v_cndmask_b32_e64 v40, v40, v28, s[6:7]
	v_bitop3_b32 v42, v38, s61, v36 bitop3:0xc8
	v_cndmask_b32_e64 v41, v41, 24, s[6:7]
	v_cmp_eq_u32_e64 s[6:7], 0, v42
	v_cmp_gt_f32_e64 s[8:9], v23, v40
	s_and_b64 s[6:7], s[6:7], s[8:9]
	v_cndmask_b32_e64 v40, v40, v23, s[6:7]
	v_bitop3_b32 v42, v38, s62, v36 bitop3:0xc8
	v_cndmask_b32_e64 v41, v41, 25, s[6:7]
	v_cmp_eq_u32_e64 s[6:7], 0, v42
	v_cmp_gt_f32_e64 s[8:9], v22, v40
	s_and_b64 s[6:7], s[6:7], s[8:9]
	v_cndmask_b32_e64 v40, v40, v22, s[6:7]
	v_bitop3_b32 v42, v38, s63, v36 bitop3:0xc8
	v_cndmask_b32_e64 v41, v41, 26, s[6:7]
	v_cmp_eq_u32_e64 s[6:7], 0, v42
	v_cmp_gt_f32_e64 s[8:9], v25, v40
	s_and_b64 s[6:7], s[6:7], s[8:9]
	v_cndmask_b32_e64 v40, v40, v25, s[6:7]
	v_bitop3_b32 v42, v38, s64, v36 bitop3:0xc8
	v_cndmask_b32_e64 v41, v41, 27, s[6:7]
	v_cmp_eq_u32_e64 s[6:7], 0, v42
	v_cmp_gt_f32_e64 s[8:9], v32, v40
	s_and_b64 s[6:7], s[6:7], s[8:9]
	v_cndmask_b32_e64 v40, v40, v32, s[6:7]
	v_bitop3_b32 v42, v38, s65, v36 bitop3:0xc8
	v_cndmask_b32_e64 v41, v41, 28, s[6:7]
	v_cmp_eq_u32_e64 s[6:7], 0, v42
	v_cmp_gt_f32_e64 s[8:9], v24, v40
	s_and_b64 s[6:7], s[6:7], s[8:9]
	v_or_b32_e32 v39, v38, v36
	v_cndmask_b32_e64 v40, v40, v24, s[6:7]
	v_bitop3_b32 v36, v38, 2.0, v36 bitop3:0xc8
	v_cndmask_b32_e64 v41, v41, 29, s[6:7]
	v_cmp_eq_u32_e64 s[6:7], 0, v36
	v_cmp_gt_f32_e64 s[8:9], v20, v40
	s_and_b64 s[6:7], s[6:7], s[8:9]
	v_cndmask_b32_e64 v38, v40, v20, s[6:7]
	v_cndmask_b32_e64 v36, v41, 30, s[6:7]
	v_cmp_lt_i32_e64 s[6:7], -1, v39
	v_cmp_gt_f32_e64 s[8:9], v21, v38
	s_and_b64 s[6:7], s[6:7], s[8:9]
	v_cndmask_b32_e64 v36, v36, 31, s[6:7]
	v_lshlrev_b32_e64 v40, v36, 1
	v_bitop3_b32 v42, v40, 1, v39 bitop3:0xc8
	v_cndmask_b32_e64 v38, v38, v21, s[6:7]
	v_cmp_eq_u32_e64 s[6:7], 0, v42
	s_and_b64 vcc, s[6:7], vcc
	v_cndmask_b32_e32 v42, v116, v51, vcc
	v_bitop3_b32 v43, v40, 2, v39 bitop3:0xc8
	v_cmp_eq_u32_e32 vcc, 0, v43
	v_cmp_gt_f32_e64 s[6:7], v15, v42
	s_and_b64 vcc, vcc, s[6:7]
	v_cndmask_b32_e32 v15, v42, v15, vcc
	v_bitop3_b32 v42, v40, 4, v39 bitop3:0xc8
	v_cndmask_b32_e64 v43, 0, 1, vcc
	v_cmp_eq_u32_e32 vcc, 0, v42
	v_cmp_gt_f32_e64 s[6:7], v14, v15
	s_and_b64 vcc, vcc, s[6:7]
	v_cndmask_b32_e32 v14, v15, v14, vcc
	v_bitop3_b32 v15, v40, 8, v39 bitop3:0xc8
	v_cndmask_b32_e64 v42, v43, 2, vcc
	v_cmp_eq_u32_e32 vcc, 0, v15
	v_cmp_gt_f32_e64 s[6:7], v17, v14
	s_and_b64 vcc, vcc, s[6:7]
	v_cndmask_b32_e32 v14, v14, v17, vcc
	v_bitop3_b32 v17, v40, 16, v39 bitop3:0xc8
	v_cndmask_b32_e64 v15, v42, 3, vcc
	v_cmp_eq_u32_e32 vcc, 0, v17
	v_cmp_gt_f32_e64 s[6:7], v16, v14
	s_and_b64 vcc, vcc, s[6:7]
	v_cndmask_b32_e32 v14, v14, v16, vcc
	v_bitop3_b32 v16, v40, 32, v39 bitop3:0xc8
	v_cndmask_b32_e64 v15, v15, 4, vcc
	v_cmp_eq_u32_e32 vcc, 0, v16
	v_cmp_gt_f32_e64 s[6:7], v11, v14
	s_and_b64 vcc, vcc, s[6:7]
	v_cndmask_b32_e32 v11, v14, v11, vcc
	v_bitop3_b32 v14, v40, 64, v39 bitop3:0xc8
	v_cndmask_b32_e64 v15, v15, 5, vcc
	v_cmp_eq_u32_e32 vcc, 0, v14
	v_cmp_gt_f32_e64 s[6:7], v10, v11
	s_and_b64 vcc, vcc, s[6:7]
	v_cndmask_b32_e32 v10, v11, v10, vcc
	v_bitop3_b32 v11, v40, s43, v39 bitop3:0xc8
	v_cndmask_b32_e64 v14, v15, 6, vcc
	v_cmp_eq_u32_e32 vcc, 0, v11
	v_cmp_gt_f32_e64 s[6:7], v13, v10
	s_and_b64 vcc, vcc, s[6:7]
	v_cndmask_b32_e32 v10, v10, v13, vcc
	v_bitop3_b32 v13, v40, s44, v39 bitop3:0xc8
; __device__ __forceinline__ void p4_router(const Params& p, Frame& F) {
;     ...
;             for (int j = 0; j < 4; ++j) { float best = -3.0e38f; int bi = 0;
; #pragma unroll
;                 for (int e = 0; e < 32; ++e) { const bool ok = !((used >> e) & 1u) && (lg[e] > best); best = ok ? lg[e] : best; bi = ok ? e : bi; }
;                 used |= 1u << bi; es[j] = bi; tv[j] = best; }
;             float den = 0.f;
; #pragma unroll
;             for (int j = 0; j < 4; ++j) { gv[j] = __expf(tv[j] - tv[0]); den += gv[j]; }
;             const float inv = 1.0f / den;
; #pragma unroll
;             for (int j = 0; j < 4; ++j) { gv[j] *= inv; lp[j] = __hip_atomic_fetch_add(&hist[es[j]], 1, __ATOMIC_RELAXED, __HIP_MEMORY_SCOPE_WORKGROUP); }
	v_cndmask_b32_e64 v11, v14, 7, vcc
	v_cmp_eq_u32_e32 vcc, 0, v13
	v_cmp_gt_f32_e64 s[6:7], v12, v10
	s_and_b64 vcc, vcc, s[6:7]
	v_cndmask_b32_e32 v10, v10, v12, vcc
	v_bitop3_b32 v12, v40, s35, v39 bitop3:0xc8
	v_cndmask_b32_e64 v11, v11, 8, vcc
	v_cmp_eq_u32_e32 vcc, 0, v12
	v_cmp_gt_f32_e64 s[6:7], v7, v10
	s_and_b64 vcc, vcc, s[6:7]
	v_cndmask_b32_e32 v7, v10, v7, vcc
	v_bitop3_b32 v10, v40, s45, v39 bitop3:0xc8
	v_cndmask_b32_e64 v11, v11, 9, vcc
	v_cmp_eq_u32_e32 vcc, 0, v10
	v_cmp_gt_f32_e64 s[6:7], v6, v7
	s_and_b64 vcc, vcc, s[6:7]
	v_cndmask_b32_e32 v6, v7, v6, vcc
	v_bitop3_b32 v7, v40, s46, v39 bitop3:0xc8
	v_cndmask_b32_e64 v10, v11, 10, vcc
	v_cmp_eq_u32_e32 vcc, 0, v7
	v_cmp_gt_f32_e64 s[6:7], v9, v6
	s_and_b64 vcc, vcc, s[6:7]
	v_cndmask_b32_e32 v6, v6, v9, vcc
	v_bitop3_b32 v9, v40, s40, v39 bitop3:0xc8
	v_cndmask_b32_e64 v7, v10, 11, vcc
	v_cmp_eq_u32_e32 vcc, 0, v9
	v_cmp_gt_f32_e64 s[6:7], v8, v6
	s_and_b64 vcc, vcc, s[6:7]
	v_cndmask_b32_e32 v6, v6, v8, vcc
	v_bitop3_b32 v8, v40, s47, v39 bitop3:0xc8
	v_cndmask_b32_e64 v7, v7, 12, vcc
	v_cmp_eq_u32_e32 vcc, 0, v8
	v_cmp_gt_f32_e64 s[6:7], v3, v6
	s_and_b64 vcc, vcc, s[6:7]
	v_cndmask_b32_e32 v3, v6, v3, vcc
	v_bitop3_b32 v6, v40, s48, v39 bitop3:0xc8
	v_cndmask_b32_e64 v7, v7, 13, vcc
	v_cmp_eq_u32_e32 vcc, 0, v6
	v_cmp_gt_f32_e64 s[6:7], v2, v3
	s_and_b64 vcc, vcc, s[6:7]
	v_cndmask_b32_e32 v2, v3, v2, vcc
	v_bitop3_b32 v3, v40, s49, v39 bitop3:0xc8
	v_cndmask_b32_e64 v6, v7, 14, vcc
	v_cmp_eq_u32_e32 vcc, 0, v3
	v_cmp_gt_f32_e64 s[6:7], v5, v2
	s_and_b64 vcc, vcc, s[6:7]
	v_cndmask_b32_e32 v2, v2, v5, vcc
	v_bitop3_b32 v5, v40, s50, v39 bitop3:0xc8
	v_cndmask_b32_e64 v3, v6, 15, vcc
	v_cmp_eq_u32_e32 vcc, 0, v5
	v_cmp_gt_f32_e64 s[6:7], v34, v2
	s_and_b64 vcc, vcc, s[6:7]
	v_cndmask_b32_e32 v2, v2, v34, vcc
	v_bitop3_b32 v5, v40, s51, v39 bitop3:0xc8
	v_cndmask_b32_e64 v3, v3, 16, vcc
	v_cmp_eq_u32_e32 vcc, 0, v5
	v_cmp_gt_f32_e64 s[6:7], v30, v2
	s_and_b64 vcc, vcc, s[6:7]
	v_cndmask_b32_e32 v2, v2, v30, vcc
	v_bitop3_b32 v5, v40, s52, v39 bitop3:0xc8
	v_cndmask_b32_e64 v3, v3, 17, vcc
	v_cmp_eq_u32_e32 vcc, 0, v5
	v_cmp_gt_f32_e64 s[6:7], v4, v2
	s_and_b64 vcc, vcc, s[6:7]
	v_cndmask_b32_e32 v2, v2, v4, vcc
	v_bitop3_b32 v4, v40, s53, v39 bitop3:0xc8
	v_cndmask_b32_e64 v3, v3, 18, vcc
	v_cmp_eq_u32_e32 vcc, 0, v4
	v_cmp_gt_f32_e64 s[6:7], v33, v2
	s_and_b64 vcc, vcc, s[6:7]
	v_cndmask_b32_e32 v2, v2, v33, vcc
	v_bitop3_b32 v4, v40, s56, v39 bitop3:0xc8
	v_cndmask_b32_e64 v3, v3, 19, vcc
	v_cmp_eq_u32_e32 vcc, 0, v4
	v_cmp_gt_f32_e64 s[6:7], v31, v2
	s_and_b64 vcc, vcc, s[6:7]
	v_cndmask_b32_e32 v2, v2, v31, vcc
	v_bitop3_b32 v4, v40, s57, v39 bitop3:0xc8
	v_cndmask_b32_e64 v3, v3, 20, vcc
	v_cmp_eq_u32_e32 vcc, 0, v4
	v_cmp_gt_f32_e64 s[6:7], v27, v2
	s_and_b64 vcc, vcc, s[6:7]
	v_cndmask_b32_e32 v2, v2, v27, vcc
	v_bitop3_b32 v4, v40, s58, v39 bitop3:0xc8
	v_cndmask_b32_e64 v3, v3, 21, vcc
	v_cmp_eq_u32_e32 vcc, 0, v4
	v_cmp_gt_f32_e64 s[6:7], v26, v2
	s_and_b64 vcc, vcc, s[6:7]
	v_cndmask_b32_e32 v2, v2, v26, vcc
	v_bitop3_b32 v4, v40, s59, v39 bitop3:0xc8
	v_cndmask_b32_e64 v3, v3, 22, vcc
	v_cmp_eq_u32_e32 vcc, 0, v4
	v_cmp_gt_f32_e64 s[6:7], v29, v2
	s_and_b64 vcc, vcc, s[6:7]
	v_cndmask_b32_e32 v2, v2, v29, vcc
	v_bitop3_b32 v4, v40, s60, v39 bitop3:0xc8
	v_cndmask_b32_e64 v3, v3, 23, vcc
	v_cmp_eq_u32_e32 vcc, 0, v4
	v_cmp_gt_f32_e64 s[6:7], v28, v2
	s_and_b64 vcc, vcc, s[6:7]
	v_cndmask_b32_e32 v2, v2, v28, vcc
	v_bitop3_b32 v4, v40, s61, v39 bitop3:0xc8
	v_cndmask_b32_e64 v3, v3, 24, vcc
	v_cmp_eq_u32_e32 vcc, 0, v4
	v_cmp_gt_f32_e64 s[6:7], v23, v2
	s_and_b64 vcc, vcc, s[6:7]
	v_cndmask_b32_e32 v2, v2, v23, vcc
	v_bitop3_b32 v4, v40, s62, v39 bitop3:0xc8
	v_cndmask_b32_e64 v3, v3, 25, vcc
	v_cmp_eq_u32_e32 vcc, 0, v4
	v_cmp_gt_f32_e64 s[6:7], v22, v2
	s_and_b64 vcc, vcc, s[6:7]
	v_cndmask_b32_e32 v2, v2, v22, vcc
	v_bitop3_b32 v4, v40, s63, v39 bitop3:0xc8
	v_cndmask_b32_e64 v3, v3, 26, vcc
	v_cmp_eq_u32_e32 vcc, 0, v4
	v_cmp_gt_f32_e64 s[6:7], v25, v2
	s_and_b64 vcc, vcc, s[6:7]
	v_cndmask_b32_e32 v2, v2, v25, vcc
	v_bitop3_b32 v4, v40, s64, v39 bitop3:0xc8
	v_cndmask_b32_e64 v3, v3, 27, vcc
	v_cmp_eq_u32_e32 vcc, 0, v4
	v_cmp_gt_f32_e64 s[6:7], v32, v2
	s_and_b64 vcc, vcc, s[6:7]
	v_cndmask_b32_e32 v2, v2, v32, vcc
	v_bitop3_b32 v4, v40, s65, v39 bitop3:0xc8
	v_cndmask_b32_e64 v3, v3, 28, vcc
	v_cmp_eq_u32_e32 vcc, 0, v4
	v_cmp_gt_f32_e64 s[6:7], v24, v2
	s_and_b64 vcc, vcc, s[6:7]
	v_cndmask_b32_e32 v2, v2, v24, vcc
	v_bitop3_b32 v4, v40, 2.0, v39 bitop3:0xc8
	v_cndmask_b32_e64 v3, v3, 29, vcc
	v_cmp_eq_u32_e32 vcc, 0, v4
	v_cmp_gt_f32_e64 s[6:7], v20, v2
	s_and_b64 vcc, vcc, s[6:7]
	v_or_b32_e32 v41, v40, v39
	v_cndmask_b32_e32 v2, v2, v20, vcc
	v_cndmask_b32_e64 v3, v3, 30, vcc
	v_cmp_lt_i32_e32 vcc, -1, v41
	v_cmp_gt_f32_e64 s[6:7], v21, v2
	s_and_b64 vcc, vcc, s[6:7]
	v_cndmask_b32_e64 v6, v3, 31, vcc
	v_cndmask_b32_e32 v3, v2, v21, vcc
	v_sub_f32_e32 v2, v35, v35
	v_mul_f32_e32 v2, 0x3fb8aa3b, v2
	v_sub_f32_e32 v5, v37, v35
	v_exp_f32_e32 v4, v2
	v_mul_f32_e32 v5, 0x3fb8aa3b, v5
	v_exp_f32_e32 v5, v5
	v_sub_f32_e32 v3, v3, v35
	v_add_f32_e32 v2, 0, v4
	v_mul_f32_e32 v3, 0x3fb8aa3b, v3
	v_add_f32_e32 v7, v2, v5
	v_sub_f32_e32 v2, v38, v35
	v_mul_f32_e32 v2, 0x3fb8aa3b, v2
	v_exp_f32_e32 v2, v2
	v_exp_f32_e32 v3, v3
	v_add_f32_e32 v7, v7, v2
	v_add_f32_e32 v7, v7, v3
	v_div_scale_f32 v8, s[6:7], v7, v7, 1.0
	v_rcp_f32_e32 v9, v8
	s_nop 0
	v_fma_f32 v10, -v8, v9, 1.0
	v_fmac_f32_e32 v9, v10, v9
	v_div_scale_f32 v10, vcc, 1.0, v7, 1.0
	v_mul_f32_e32 v11, v10, v9
	v_fma_f32 v12, -v8, v11, v10
	v_fmac_f32_e32 v11, v12, v9
	v_fma_f32 v8, -v8, v11, v10
	v_div_fmas_f32 v8, v8, v9, v11
	v_div_fixup_f32 v12, v8, v7, 1.0
	v_lshl_add_u32 v7, v18, 2, s37
	ds_add_rtn_u32 v10, v7, v114
	v_lshl_add_u32 v7, v19, 2, s37
	ds_add_rtn_u32 v9, v7, v114
	v_lshl_add_u32 v7, v36, 2, s37
	ds_add_rtn_u32 v8, v7, v114
	v_lshl_add_u32 v7, v6, 2, s37
	ds_add_rtn_u32 v7, v7, v114
	v_pk_mul_f32 v[2:3], v[2:3], v[12:13] op_sel_hi:[1,0]
	v_pk_mul_f32 v[4:5], v[4:5], v[12:13] op_sel_hi:[1,0]

; __device__ __forceinline__ void p7_final(const Params& p, Frame& F) {
;     ...
;     for (int i = F.tid; i < DM; i += 512) fwl[i] = fw[i];
;     __syncthreads();
;     if (gw >= T_TOK) return;
;     f32x4 v[8], nv[8]; i32x4 me, mp, nme, nmp; f32x4 mg, nmg;
;     ...
;     P7_LOAD(v, me, mp, mg, gw);
;     for (int t = gw; t < T_TOK; t += NGW) {
;         u32x2 y[4][4];
; #pragma unroll
;         for (int j = 0; j < 4; ++j) { const size_t slot = (size_t)tile0[me[j]] * 256 + mp[j];
.LBB0_1070:
	global_load_dword v4, v[2:3], off
	v_add_u32_e32 v0, 0x200, v0
	v_cmp_lt_u32_e32 vcc, s4, v0
	v_lshl_add_u64 v[2:3], v[2:3], 0, s[2:3]
	s_or_b64 s[0:1], vcc, s[0:1]
	s_waitcnt vmcnt(0)
	ds_write_b32 v1, v4
	v_add_u32_e32 v1, 0x800, v1
	s_andn2_b64 exec, exec, s[0:1]
	s_cbranch_execnz .LBB0_1070
	s_or_b64 exec, exec, s[0:1]
	s_lshl_b32 s0, s90, 3
	s_add_i32 s14, s0, s54
	s_cmpk_lt_i32 s14, 0x4000
	s_waitcnt lgkmcnt(0)
	s_barrier
	s_cbranch_scc0 .LBB0_1074
	s_add_u32 s4, s96, 0x4f800000
	s_addc_u32 s5, s97, 0
	s_lshl_b32 s6, s94, 3
	s_add_u32 s0, s96, 0x31800000
	s_addc_u32 s1, s97, 0
	s_add_u32 s16, s96, 0x1a0000
	s_addc_u32 s17, s97, 0
	s_add_u32 s18, s96, 0x1e0000
	s_addc_u32 s19, s97, 0
	s_add_u32 s20, s96, 0x220000
	s_addc_u32 s21, s97, 0
	s_ashr_i32 s15, s14, 31
	s_lshl_b64 s[2:3], s[14:15], 13
	s_add_u32 s8, s0, s2
	s_addc_u32 s9, s1, s3
	s_lshl_b32 s10, s14, 2
	s_ashr_i32 s11, s10, 31
	s_lshl_b64 s[12:13], s[10:11], 2
	v_mov_b32_e32 v77, 0
	s_add_u32 s10, s20, s12
	v_lshlrev_b32_e32 v34, 5, v162
	v_mov_b32_e32 v35, v77
	s_addc_u32 s11, s21, s13
	v_lshl_add_u64 v[20:21], s[8:9], 0, v[34:35]
	s_movk_i32 s15, 0x1000
	s_add_u32 s22, s18, s12
	global_load_dwordx4 v[36:39], v34, s[8:9] nt
	global_load_dwordx4 v[0:3], v34, s[8:9] offset:16 nt
	global_load_dwordx4 v[4:7], v34, s[8:9] offset:2048 nt
	global_load_dwordx4 v[8:11], v34, s[8:9] offset:2064 nt
	s_mov_b64 s[8:9], 0x1000
	s_addc_u32 s23, s19, s13
	global_load_dwordx4 v[12:15], v77, s[10:11] nt
	global_load_dwordx4 v[40:43], v77, s[22:23] nt
	v_add_co_u32_e32 v24, vcc, s15, v20
	s_mov_b64 s[10:11], 0x1800
	v_lshl_add_u64 v[22:23], v[20:21], 0, s[8:9]
	v_addc_co_u32_e32 v25, vcc, 0, v21, vcc
	v_lshl_add_u64 v[20:21], v[20:21], 0, s[10:11]
	s_add_u32 s12, s16, s12
	global_load_dwordx4 v[16:19], v[24:25], off nt
	global_load_dwordx4 v[44:47], v[22:23], off offset:16 nt
	s_addc_u32 s13, s17, s13
	global_load_dwordx4 v[24:27], v[24:25], off offset:2048 nt
	v_mbcnt_hi_u32_b32 v32, -1, v32
	global_load_dwordx4 v[20:23], v[20:21], off offset:16 nt
	v_and_b32_e32 v33, 64, v32
	global_load_dwordx4 v[28:31], v77, s[12:13] nt
	v_xor_b32_e32 v48, 1, v32
	v_add_u32_e32 v33, 64, v33
	v_xor_b32_e32 v49, 2, v32
	v_cmp_lt_i32_e32 vcc, v48, v33
	v_xor_b32_e32 v50, 4, v32
	v_xor_b32_e32 v51, 8, v32
	v_cndmask_b32_e32 v48, v32, v48, vcc
	v_cmp_lt_i32_e32 vcc, v49, v33
	v_xor_b32_e32 v52, 16, v32
	v_readlane_b32 s24, v245, 0
	v_cndmask_b32_e32 v49, v32, v49, vcc
	v_cmp_lt_i32_e32 vcc, v50, v33
	v_xor_b32_e32 v53, 32, v32
	v_readlane_b32 s26, v245, 2
	v_cndmask_b32_e32 v50, v32, v50, vcc
	v_cmp_lt_i32_e32 vcc, v51, v33
	v_lshl_add_u64 v[78:79], s[0:1], 0, v[34:35]
	v_readlane_b32 s27, v245, 3
	v_cndmask_b32_e32 v51, v32, v51, vcc
	v_cmp_lt_i32_e32 vcc, v52, v33
	s_add_u32 s0, s26, s2
	s_addc_u32 s1, s27, s3
	v_cndmask_b32_e32 v52, v32, v52, vcc
	v_cmp_lt_i32_e32 vcc, v53, v33
	v_readlane_b32 s25, v245, 1
	s_ashr_i32 s7, s6, 31
	v_cndmask_b32_e32 v32, v32, v53, vcc
	v_lshlrev_b32_e32 v225, 2, v32
	v_lshl_add_u64 v[32:33], s[0:1], 0, v[34:35]
	v_lshlrev_b32_e32 v76, 3, v162
	v_mov_b32_e32 v218, 0x358637bd
	s_mov_b32 s22, 0xf800000
	v_mov_b32_e32 v219, 0x260
	v_lshlrev_b32_e32 v220, 2, v48
	v_lshlrev_b32_e32 v221, 2, v49
	v_lshlrev_b32_e32 v222, 2, v50
	v_lshlrev_b32_e32 v223, 2, v51
	v_lshlrev_b32_e32 v224, 2, v52
	s_add_i32 s23, 0, 0x27d00
	s_lshl_b64 s[12:13], s[6:7], 13
	v_lshl_add_u64 v[80:81], v[32:33], 0, s[8:9]
	s_waitcnt vmcnt(9)
	v_mov_b32_e32 v82, v1
	v_mov_b32_e32 v1, v2
	v_mov_b32_e32 v83, v3
	s_waitcnt vmcnt(8)
	v_mov_b32_e32 v2, v5
	v_mov_b32_e32 v5, v6
	v_mov_b32_e32 v3, v7
	s_waitcnt vmcnt(7)
	v_mov_b32_e32 v6, v9
	s_waitcnt vmcnt(5)
	v_readfirstlane_b32 s26, v40
	v_readfirstlane_b32 s25, v41
	v_readfirstlane_b32 s24, v42
	v_readfirstlane_b32 s7, v43
	v_mov_b32_e32 v9, v10
	v_mov_b32_e32 v7, v11
	s_waitcnt vmcnt(3)
	v_mov_b32_e32 v10, v45
	v_mov_b32_e32 v11, v46
	s_waitcnt vmcnt(2)
	v_mov_b32_e32 v86, v25
	v_mov_b32_e32 v87, v27
	s_waitcnt vmcnt(1)
	v_mov_b32_e32 v85, v21
	v_mov_b32_e32 v25, v22
	v_mov_b32_e32 v27, v23
.LBB0_1073:
	s_waitcnt vmcnt(0)
	v_lshlrev_b32_e32 v21, 2, v28
	s_ashr_i32 s1, s26, 31
	s_mov_b32 s0, s26
	s_ashr_i32 s27, s25, 31
	s_mov_b32 s26, s25
	s_ashr_i32 s25, s24, 31
	s_ashr_i32 s29, s7, 31
	s_mov_b32 s28, s7
	v_lshlrev_b32_e32 v22, 2, v29
	v_lshlrev_b32_e32 v23, 2, v30
	v_lshlrev_b32_e32 v28, 2, v31
	s_add_i32 s2, s14, s6
	v_add_u32_e32 v21, s23, v21
	s_lshl_b64 s[30:31], s[0:1], 11
	s_lshl_b64 s[26:27], s[26:27], 11
	s_lshl_b64 s[24:25], s[24:25], 11
	s_lshl_b64 s[28:29], s[28:29], 11
	v_add_u32_e32 v29, s23, v22
	v_add_u32_e32 v23, s23, v23
	v_add_u32_e32 v31, s23, v28
	ds_read_b32 v22, v21
	ds_read_b32 v28, v29
	ds_read_b32 v30, v23
	ds_read_b32 v32, v31
	s_cmpk_lt_i32 s2, 0x4000
	s_cselect_b64 s[0:1], -1, 0
	s_and_b64 s[34:35], s[0:1], exec
	s_cselect_b32 s34, s2, s14
	s_lshl_b32 s36, s34, 2
	s_waitcnt lgkmcnt(3)
	v_ashrrev_i32_e32 v23, 31, v22
	s_waitcnt lgkmcnt(2)
	v_ashrrev_i32_e32 v29, 31, v28
	s_waitcnt lgkmcnt(1)
	v_ashrrev_i32_e32 v31, 31, v30
	s_waitcnt lgkmcnt(0)
; __device__ __forceinline__ void p7_final(const Params& p, Frame& F) {
;     ...
;     P7_LOAD(v, me, mp, mg, gw);
;     for (int t = gw; t < T_TOK; t += NGW) {
;         u32x2 y[4][4];
; #pragma unroll
;         for (int j = 0; j < 4; ++j) { const size_t slot = (size_t)tile0[me[j]] * 256 + mp[j];
; #pragma unroll
;             for (int i = 0; i < 4; ++i) y[j][i] = *(const u32x2*)(ys + slot * DM + 512 * i + 8 * lane); }
;         const int tn = (t + NGW < T_TOK) ? t + NGW : t;
;         P7_LOAD(nv, nme, nmp, nmg, tn);
; #pragma unroll
;         for (int j = 0; j < 4; ++j) { const float g = mg[j]; __builtin_amdgcn_sched_barrier(0);
; #pragma unroll
;             for (int i = 0; i < 4; ++i) {
;                 const f32x2_t a0 = __builtin_amdgcn_cvt_pk_f32_fp8(y[j][i].x, false), a1 = __builtin_amdgcn_cvt_pk_f32_fp8(y[j][i].x, true), a2 = __builtin_amdgcn_cvt_pk_f32_fp8(y[j][i].y, false), a3 = __builtin_amdgcn_cvt_pk_f32_fp8(y[j][i].y, true);
;                 v[2 * i][0] += g * a0.x; v[2 * i][1] += g * a0.y; v[2 * i][2] += g * a1.x; v[2 * i][3] += g * a1.y;
;                 v[2 * i + 1][0] += g * a2.x; v[2 * i + 1][1] += g * a2.y; v[2 * i + 1][2] += g * a3.x; v[2 * i + 1][3] += g * a3.y; } }
	v_ashrrev_i32_e32 v33, 31, v32
	s_ashr_i32 s37, s36, 31
	v_lshlrev_b64 v[22:23], 19, v[22:23]
	v_lshlrev_b64 v[28:29], 19, v[28:29]
	v_lshlrev_b64 v[30:31], 19, v[30:31]
	v_lshlrev_b64 v[32:33], 19, v[32:33]
	s_lshl_b64 s[36:37], s[36:37], 2
	v_lshl_add_u64 v[22:23], s[4:5], 0, v[22:23]
	v_lshl_add_u64 v[28:29], s[4:5], 0, v[28:29]
	v_lshl_add_u64 v[30:31], s[4:5], 0, v[30:31]
	v_lshl_add_u64 v[32:33], s[4:5], 0, v[32:33]
	s_add_u32 s38, s16, s36
	v_lshl_add_u64 v[22:23], v[22:23], 0, s[30:31]
	v_lshl_add_u64 v[28:29], v[28:29], 0, s[26:27]
	v_lshl_add_u64 v[30:31], v[30:31], 0, s[24:25]
	v_lshl_add_u64 v[32:33], v[32:33], 0, s[28:29]
	s_addc_u32 s39, s17, s37
	v_lshl_add_u64 v[22:23], v[22:23], 0, v[76:77]
	v_lshl_add_u64 v[34:35], v[28:29], 0, v[76:77]
	v_lshl_add_u64 v[40:41], v[30:31], 0, v[76:77]
	v_lshl_add_u64 v[32:33], v[32:33], 0, v[76:77]
	global_load_dwordx4 v[28:31], v77, s[38:39] nt
	global_load_dwordx2 v[92:93], v[22:23], off nt
	global_load_dwordx2 v[94:95], v[22:23], off offset:512 nt
	global_load_dwordx2 v[102:103], v[22:23], off offset:1024 nt
	global_load_dwordx2 v[104:105], v[22:23], off offset:1536 nt
	global_load_dwordx2 v[106:107], v[34:35], off nt
	global_load_dwordx2 v[108:109], v[34:35], off offset:512 nt
	global_load_dwordx2 v[110:111], v[34:35], off offset:1024 nt
	global_load_dwordx2 v[118:119], v[34:35], off offset:1536 nt
	global_load_dwordx2 v[120:121], v[40:41], off nt
	global_load_dwordx2 v[122:123], v[40:41], off offset:512 nt
	global_load_dwordx2 v[124:125], v[40:41], off offset:1024 nt
	global_load_dwordx2 v[126:127], v[40:41], off offset:1536 nt
	global_load_dwordx2 v[128:129], v[32:33], off nt
	global_load_dwordx2 v[142:143], v[32:33], off offset:512 nt
	global_load_dwordx2 v[148:149], v[32:33], off offset:1024 nt
	global_load_dwordx2 v[176:177], v[32:33], off offset:1536 nt
	s_add_u32 s24, s18, s36
	s_addc_u32 s25, s19, s37
	global_load_dwordx4 v[88:91], v77, s[24:25] nt
	s_add_u32 s24, s20, s36
	s_addc_u32 s25, s21, s37
	s_ashr_i32 s35, s34, 31
	global_load_dwordx4 v[32:35], v77, s[24:25] nt
	s_lshl_b64 s[24:25], s[34:35], 13
	v_lshl_add_u64 v[22:23], v[78:79], 0, s[24:25]
	v_add_co_u32_e32 v42, vcc, s15, v22
	v_lshl_add_u64 v[40:41], v[22:23], 0, s[8:9]
	s_nop 0
	v_addc_co_u32_e32 v43, vcc, 0, v23, vcc
	global_load_dwordx4 v[72:75], v[22:23], off nt
	global_load_dwordx4 v[48:51], v[22:23], off offset:16 nt
	global_load_dwordx4 v[52:55], v[22:23], off offset:2048 nt
	global_load_dwordx4 v[56:59], v[22:23], off offset:2064 nt
	v_lshl_add_u64 v[22:23], v[22:23], 0, s[10:11]
	global_load_dwordx4 v[68:71], v[42:43], off nt
	global_load_dwordx4 v[64:67], v[40:41], off offset:16 nt
	global_load_dwordx4 v[60:63], v[42:43], off offset:2048 nt
	s_nop 0
	global_load_dwordx4 v[40:43], v[22:23], off offset:16 nt
	s_waitcnt vmcnt(9)
	v_readfirstlane_b32 s26, v88
	v_readfirstlane_b32 s25, v89
	v_readfirstlane_b32 s24, v90
	v_readfirstlane_b32 s7, v91
	v_cvt_pk_f32_fp8_e32 v[132:133], v104
	v_cvt_pk_f32_fp8_sdwa v[134:135], v104 src0_sel:WORD_1
	v_cvt_pk_f32_fp8_e32 v[162:163], v105
	v_cvt_pk_f32_fp8_e32 v[154:155], v92
	v_fmac_f32_e32 v24, v12, v132
	v_fmac_f32_e32 v26, v12, v134
	v_cvt_pk_f32_fp8_sdwa v[156:157], v92 src0_sel:WORD_1
	v_cvt_pk_f32_fp8_e32 v[188:189], v93
	v_cvt_pk_f32_fp8_sdwa v[96:97], v93 src0_sel:WORD_1
	v_cvt_pk_f32_fp8_e32 v[198:199], v94
	v_cvt_pk_f32_fp8_sdwa v[98:99], v94 src0_sel:WORD_1
	v_cvt_pk_f32_fp8_e32 v[206:207], v95
	v_cvt_pk_f32_fp8_sdwa v[100:101], v95 src0_sel:WORD_1
	v_cvt_pk_f32_fp8_e32 v[22:23], v102
	v_cvt_pk_f32_fp8_sdwa v[202:203], v102 src0_sel:WORD_1
	v_cvt_pk_f32_fp8_e32 v[88:89], v103
	v_cvt_pk_f32_fp8_sdwa v[130:131], v103 src0_sel:WORD_1
	v_cvt_pk_f32_fp8_sdwa v[194:195], v105 src0_sel:WORD_1
	v_mul_f32_e32 v21, v12, v162
	v_cvt_pk_f32_fp8_e32 v[102:103], v110
	v_cvt_pk_f32_fp8_e32 v[104:105], v111
	v_cvt_pk_f32_fp8_e32 v[112:113], v106
	v_cvt_pk_f32_fp8_sdwa v[114:115], v106 src0_sel:WORD_1
	v_cvt_pk_f32_fp8_e32 v[200:201], v107
	v_cvt_pk_f32_fp8_sdwa v[90:91], v107 src0_sel:WORD_1
	v_cvt_pk_f32_fp8_sdwa v[106:107], v111 src0_sel:WORD_1
	v_cvt_pk_f32_fp8_e32 v[208:209], v108
	v_cvt_pk_f32_fp8_sdwa v[92:93], v108 src0_sel:WORD_1
	v_cvt_pk_f32_fp8_e32 v[212:213], v109
	v_cvt_pk_f32_fp8_sdwa v[94:95], v109 src0_sel:WORD_1
	v_mov_b32_e32 v108, v22
	v_mov_b32_e32 v109, v102
	v_mov_b32_e32 v102, v23
	v_mov_b32_e32 v22, v88
	v_mov_b32_e32 v23, v104
	v_pk_mul_f32 v[22:23], v[12:13], v[22:23]
	v_cvt_pk_f32_fp8_e32 v[166:167], v118
	v_add_f32_e32 v22, v44, v22
	v_add_f32_e32 v84, v22, v23
	v_mov_b32_e32 v22, v130
	v_mov_b32_e32 v23, v106
	v_mov_b32_e32 v106, v131
	v_cvt_pk_f32_fp8_sdwa v[164:165], v118 src0_sel:WORD_1
	v_cvt_pk_f32_fp8_sdwa v[116:117], v110 src0_sel:WORD_1
	v_pk_mul_f32 v[110:111], v[12:13], v[22:23]
	v_pk_mul_f32 v[22:23], v[12:13], v[106:107]
	v_cvt_pk_f32_fp8_e32 v[44:45], v119
	v_add_f32_e32 v22, v47, v22
	v_add_f32_e32 v88, v22, v23
	v_mov_b32_e32 v22, v133
	v_mov_b32_e32 v23, v167
	v_mov_b32_e32 v104, v89
	v_pk_mul_f32 v[190:191], v[12:13], v[22:23]
	v_mov_b32_e32 v22, v135
	v_mov_b32_e32 v23, v165
	v_pk_mul_f32 v[108:109], v[12:13], v[108:109]
	v_pk_mul_f32 v[102:103], v[12:13], v[102:103]
	v_pk_mul_f32 v[172:173], v[12:13], v[104:105]
	v_cvt_pk_f32_fp8_sdwa v[216:217], v119 src0_sel:WORD_1
	v_pk_mul_f32 v[136:137], v[12:13], v[22:23]
	v_mul_f32_e32 v226, v13, v44
	v_cvt_pk_f32_fp8_e32 v[22:23], v127
	v_cvt_pk_f32_fp8_e32 v[150:151], v120
	v_cvt_pk_f32_fp8_sdwa v[152:153], v120 src0_sel:WORD_1
	v_cvt_pk_f32_fp8_e32 v[204:205], v121
	v_cvt_pk_f32_fp8_sdwa v[130:131], v121 src0_sel:WORD_1
	v_cvt_pk_f32_fp8_e32 v[210:211], v122
; __device__ __forceinline__ void p7_final(const Params& p, Frame& F) {
;     ...
;         for (int j = 0; j < 4; ++j) { const float g = mg[j]; __builtin_amdgcn_sched_barrier(0);
; #pragma unroll
;             for (int i = 0; i < 4; ++i) {
;                 const f32x2_t a0 = __builtin_amdgcn_cvt_pk_f32_fp8(y[j][i].x, false), a1 = __builtin_amdgcn_cvt_pk_f32_fp8(y[j][i].x, true), a2 = __builtin_amdgcn_cvt_pk_f32_fp8(y[j][i].y, false), a3 = __builtin_amdgcn_cvt_pk_f32_fp8(y[j][i].y, true);
;                 v[2 * i][0] += g * a0.x; v[2 * i][1] += g * a0.y; v[2 * i][2] += g * a1.x; v[2 * i][3] += g * a1.y;
;                 v[2 * i + 1][0] += g * a2.x; v[2 * i + 1][1] += g * a2.y; v[2 * i + 1][2] += g * a3.x; v[2 * i + 1][3] += g * a3.y; } }
	v_cvt_pk_f32_fp8_sdwa v[132:133], v122 src0_sel:WORD_1
	v_cvt_pk_f32_fp8_e32 v[214:215], v123
	v_cvt_pk_f32_fp8_sdwa v[134:135], v123 src0_sel:WORD_1
	v_cvt_pk_f32_fp8_e32 v[118:119], v124
	v_cvt_pk_f32_fp8_sdwa v[158:159], v124 src0_sel:WORD_1
	v_cvt_pk_f32_fp8_e32 v[170:171], v125
	v_cvt_pk_f32_fp8_sdwa v[120:121], v125 src0_sel:WORD_1
	v_cvt_pk_f32_fp8_e32 v[146:147], v126
	v_cvt_pk_f32_fp8_sdwa v[144:145], v126 src0_sel:WORD_1
	v_cvt_pk_f32_fp8_sdwa v[106:107], v127 src0_sel:WORD_1
	v_mul_f32_e32 v89, v14, v23
	v_cvt_pk_f32_fp8_e32 v[126:127], v129
	v_cvt_pk_f32_fp8_sdwa v[104:105], v129 src0_sel:WORD_1
	v_pk_fma_f32 v[178:179], v[12:13], v[154:155], v[36:37] op_sel_hi:[0,1,1]
	v_pk_fma_f32 v[182:183], v[12:13], v[156:157], v[38:39] op_sel_hi:[0,1,1]
	v_cvt_pk_f32_fp8_e32 v[154:155], v142
	v_cvt_pk_f32_fp8_sdwa v[122:123], v142 src0_sel:WORD_1
	v_cvt_pk_f32_fp8_e32 v[156:157], v143
	v_cvt_pk_f32_fp8_sdwa v[124:125], v143 src0_sel:WORD_1
	v_cvt_pk_f32_fp8_e32 v[142:143], v148
	v_cvt_pk_f32_fp8_e32 v[138:139], v128
	v_cvt_pk_f32_fp8_sdwa v[140:141], v128 src0_sel:WORD_1
	v_cvt_pk_f32_fp8_sdwa v[160:161], v148 src0_sel:WORD_1
	v_cvt_pk_f32_fp8_e32 v[128:129], v149
	v_cvt_pk_f32_fp8_sdwa v[148:149], v149 src0_sel:WORD_1
	v_mov_b32_e32 v184, v108
	v_mov_b32_e32 v185, v102
	v_mov_b32_e32 v186, v172
	v_mov_b32_e32 v187, v110
	v_mov_b32_e32 v110, v173
	v_cvt_pk_f32_fp8_e32 v[174:175], v176
	v_cvt_pk_f32_fp8_sdwa v[172:173], v176 src0_sel:WORD_1
	v_mov_b32_e32 v196, v188
	v_mov_b32_e32 v197, v96
	v_mov_b32_e32 v96, v189
	v_mov_b32_e32 v188, v204
	v_mov_b32_e32 v189, v130
	v_mov_b32_e32 v130, v205
	v_mov_b32_e32 v204, v198
	v_mov_b32_e32 v205, v98
	v_mov_b32_e32 v98, v199
	v_mov_b32_e32 v198, v210
	v_mov_b32_e32 v199, v132
	v_mov_b32_e32 v132, v211
	v_mov_b32_e32 v210, v206
	v_mov_b32_e32 v211, v100
	v_mov_b32_e32 v100, v207
	v_mov_b32_e32 v162, v118
	v_mov_b32_e32 v118, v171
	v_mov_b32_e32 v192, v190
	v_mov_b32_e32 v193, v136
	v_mov_b32_e32 v136, v191
	v_mov_b32_e32 v190, v200
	v_mov_b32_e32 v191, v90
	v_mov_b32_e32 v90, v201
	v_mov_b32_e32 v200, v208
	v_mov_b32_e32 v201, v92
	v_mov_b32_e32 v92, v209
	v_mov_b32_e32 v208, v212
	v_mov_b32_e32 v209, v94
	v_mov_b32_e32 v94, v213
	v_pk_fma_f32 v[212:213], v[12:13], v[202:203], v[18:19] op_sel_hi:[0,1,1]
	v_mov_b32_e32 v167, v194
	v_mov_b32_e32 v165, v195
	v_mov_b32_e32 v171, v163
	v_mov_b32_e32 v163, v76
	s_waitcnt vmcnt(7)
	v_mov_b32_e32 v36, v72
	v_mov_b32_e32 v37, v73
	v_mov_b32_e32 v38, v74
	v_mov_b32_e32 v39, v75
	s_waitcnt vmcnt(3)
	v_mov_b32_e32 v18, v70
	v_mov_b32_e32 v19, v71
	v_pk_fma_f32 v[70:71], v[12:13], v[112:113], v[178:179] op_sel:[1,0,0]
	v_pk_fma_f32 v[72:73], v[12:13], v[114:115], v[182:183] op_sel:[1,0,0]
	v_pk_add_f32 v[74:75], v[16:17], v[184:185]
	v_pk_fma_f32 v[178:179], v[12:13], v[196:197], v[0:1] op_sel_hi:[0,1,1]
	v_pk_fma_f32 v[96:97], v[12:13], v[96:97], v[82:83] op_sel_hi:[0,1,1]
	v_pk_fma_f32 v[182:183], v[12:13], v[204:205], v[4:5] op_sel_hi:[0,1,1]
	v_pk_fma_f32 v[98:99], v[12:13], v[98:99], v[2:3] op_sel_hi:[0,1,1]
	v_pk_fma_f32 v[184:185], v[12:13], v[210:211], v[8:9] op_sel_hi:[0,1,1]
	v_pk_fma_f32 v[100:101], v[12:13], v[100:101], v[6:7] op_sel_hi:[0,1,1]
	v_mov_b32_e32 v176, v145
	v_mov_b32_e32 v206, v214
	v_mov_b32_e32 v207, v134
	v_mov_b32_e32 v134, v215
	v_mov_b32_e32 v214, v14
	v_mov_b32_e32 v215, v12
	v_mov_b32_e32 v145, v217
	v_pk_fma_f32 v[116:117], v[12:13], v[116:117], v[212:213] op_sel:[1,0,0]
	v_pk_fma_f32 v[166:167], v[12:13], v[166:167], v[24:25] op_sel:[1,0,0] op_sel_hi:[0,1,1]
	v_pk_fma_f32 v[164:165], v[12:13], v[164:165], v[26:27] op_sel:[1,0,0] op_sel_hi:[0,1,1]
	v_mov_b32_e32 v0, v48
	v_mov_b32_e32 v82, v49
	v_mov_b32_e32 v1, v50
	v_mov_b32_e32 v83, v51
	v_mov_b32_e32 v4, v52
	v_mov_b32_e32 v2, v53
	v_mov_b32_e32 v5, v54
	v_mov_b32_e32 v3, v55
	v_mov_b32_e32 v8, v56
	v_mov_b32_e32 v6, v57
	v_mov_b32_e32 v9, v58
	v_mov_b32_e32 v7, v59
	v_pk_fma_f32 v[48:49], v[12:13], v[190:191], v[178:179] op_sel:[1,0,0]
	v_pk_fma_f32 v[50:51], v[12:13], v[90:91], v[96:97] op_sel:[1,0,0]
	v_pk_fma_f32 v[52:53], v[12:13], v[200:201], v[182:183] op_sel:[1,0,0]
	v_pk_fma_f32 v[54:55], v[12:13], v[92:93], v[98:99] op_sel:[1,0,0]
	v_pk_fma_f32 v[56:57], v[12:13], v[208:209], v[184:185] op_sel:[1,0,0]
	v_pk_fma_f32 v[58:59], v[12:13], v[94:95], v[100:101] op_sel:[1,0,0]
	v_mov_b32_e32 v12, v14
	v_mov_b32_e32 v46, v15
	v_mov_b32_e32 v168, v120
	v_cvt_pk_f32_fp8_sdwa v[180:181], v177 src0_sel:WORD_1
	v_mov_b32_e32 v120, v147
	v_mov_b32_e32 v147, v216
	s_waitcnt vmcnt(2)
	v_mov_b32_e32 v47, v67
	v_pk_add_f32 v[112:113], v[10:11], v[186:187]
	v_pk_add_f32 v[114:115], v[86:87], v[192:193]
	v_pk_fma_f32 v[170:171], v[214:215], v[170:171], v[84:85]
	s_waitcnt vmcnt(0)
; __device__ __forceinline__ void p7_final(const Params& p, Frame& F) {
;     ...
;         for (int j = 0; j < 4; ++j) { const float g = mg[j]; __builtin_amdgcn_sched_barrier(0);
; #pragma unroll
;             for (int i = 0; i < 4; ++i) {
;                 const f32x2_t a0 = __builtin_amdgcn_cvt_pk_f32_fp8(y[j][i].x, false), a1 = __builtin_amdgcn_cvt_pk_f32_fp8(y[j][i].x, true), a2 = __builtin_amdgcn_cvt_pk_f32_fp8(y[j][i].y, false), a3 = __builtin_amdgcn_cvt_pk_f32_fp8(y[j][i].y, true);
;                 v[2 * i][0] += g * a0.x; v[2 * i][1] += g * a0.y; v[2 * i][2] += g * a1.x; v[2 * i][3] += g * a1.y;
;                 v[2 * i + 1][0] += g * a2.x; v[2 * i + 1][1] += g * a2.y; v[2 * i + 1][2] += g * a3.x; v[2 * i + 1][3] += g * a3.y; } }
;         float s = 0.f;
; #pragma unroll
;         for (int i = 0; i < 8; ++i) s += (v[i][0] * v[i][0] + v[i][1] * v[i][1]) + (v[i][2] * v[i][2] + v[i][3] * v[i][3]);
	v_mov_b32_e32 v85, v41
	v_mov_b32_e32 v25, v42
	v_mov_b32_e32 v27, v43
	v_pk_fma_f32 v[42:43], v[14:15], v[150:151], v[70:71] op_sel_hi:[0,1,1]
	v_pk_fma_f32 v[150:151], v[14:15], v[152:153], v[72:73] op_sel_hi:[0,1,1]
	v_lshl_add_u32 v41, v163, 2, 0
	v_pk_fma_f32 v[98:99], v[14:15], v[130:131], v[50:51] op_sel_hi:[0,1,1]
	v_pk_fma_f32 v[130:131], v[14:15], v[134:135], v[58:59] op_sel_hi:[0,1,1]
	v_pk_fma_f32 v[134:135], v[12:13], v[144:145], v[164:165]
	v_mov_b32_e32 v163, v142
	v_mov_b32_e32 v142, v119
	v_mov_b32_e32 v145, v104
	v_mov_b32_e32 v104, v127
	v_mov_b32_e32 v102, v109
	v_cvt_pk_f32_fp8_e32 v[108:109], v177
	v_pk_add_f32 v[110:111], v[112:113], v[110:111]
	v_pk_add_f32 v[112:113], v[114:115], v[136:137]
	v_pk_fma_f32 v[94:95], v[14:15], v[158:159], v[116:117] op_sel_hi:[0,1,1]
	v_pk_fma_f32 v[96:97], v[14:15], v[188:189], v[48:49] op_sel_hi:[0,1,1]
	v_pk_fma_f32 v[114:115], v[14:15], v[132:133], v[54:55] op_sel_hi:[0,1,1]
	v_pk_fma_f32 v[116:117], v[14:15], v[206:207], v[56:57] op_sel_hi:[0,1,1]
	v_pk_fma_f32 v[132:133], v[12:13], v[146:147], v[166:167]
	v_mov_b32_e32 v12, v15
	v_pk_fma_f32 v[42:43], v[46:47], v[138:139], v[42:43] op_sel_hi:[0,1,1]
	v_pk_fma_f32 v[136:137], v[46:47], v[140:141], v[150:151] op_sel_hi:[0,1,1]
	v_mov_b32_e32 v119, v129
	v_mov_b32_e32 v169, v148
	v_mov_b32_e32 v148, v121
	v_mov_b32_e32 v121, v175
	v_mov_b32_e32 v177, v173
	v_mov_b32_e32 v144, v126
	v_mov_b32_e32 v127, v122
	v_mov_b32_e32 v122, v155
	v_mov_b32_e32 v146, v156
	v_mov_b32_e32 v147, v124
	v_mov_b32_e32 v124, v157
	v_mov_b32_e32 v129, v45
	v_mov_b32_e32 v175, v106
	v_mov_b32_e32 v173, v107
	v_pk_mul_f32 v[106:107], v[14:15], v[162:163]
	v_pk_mul_f32 v[142:143], v[14:15], v[142:143]
	v_pk_fma_f32 v[98:99], v[46:47], v[104:105], v[98:99] op_sel_hi:[0,1,1]
	v_pk_add_f32 v[102:103], v[74:75], v[102:103]
	v_pk_fma_f32 v[100:101], v[14:15], v[198:199], v[52:53] op_sel_hi:[0,1,1]
	v_mov_b32_e32 v126, v154
	v_pk_mul_f32 v[118:119], v[14:15], v[118:119]
	v_pk_mul_f32 v[150:151], v[14:15], v[168:169]
	v_pk_mul_f32 v[120:121], v[14:15], v[120:121]
	v_pk_mul_f32 v[152:153], v[14:15], v[176:177]
	v_mul_f32_e32 v84, v43, v43
	v_pk_fma_f32 v[96:97], v[46:47], v[144:145], v[96:97] op_sel_hi:[0,1,1]
	v_pk_fma_f32 v[104:105], v[46:47], v[122:123], v[114:115] op_sel_hi:[0,1,1]
	v_pk_fma_f32 v[114:115], v[46:47], v[146:147], v[116:117] op_sel_hi:[0,1,1]
	v_pk_fma_f32 v[116:117], v[46:47], v[124:125], v[130:131] op_sel_hi:[0,1,1]
	v_pk_fma_f32 v[122:123], v[12:13], v[128:129], v[170:171]
	v_mul_f32_e32 v12, v137, v137
	v_mov_b32_e32 v128, v106
	v_mov_b32_e32 v129, v142
	v_pk_mul_f32 v[130:131], v[98:99], v[98:99]
	v_pk_fma_f32 v[94:95], v[46:47], v[160:161], v[94:95] op_sel_hi:[0,1,1]
	v_pk_mul_f32 v[148:149], v[14:15], v[148:149]
	v_pk_fma_f32 v[100:101], v[46:47], v[126:127], v[100:101] op_sel_hi:[0,1,1]
	v_pk_fma_f32 v[124:125], v[14:15], v[174:175], v[132:133] op_sel:[1,0,0] op_sel_hi:[0,1,1]
	v_pk_fma_f32 v[126:127], v[14:15], v[172:173], v[134:135] op_sel:[1,0,0] op_sel_hi:[0,1,1]
	v_mov_b32_e32 v142, v107
	v_mov_b32_e32 v106, v118
	v_mov_b32_e32 v107, v150
	v_mov_b32_e32 v150, v119
	v_mov_b32_e32 v118, v120
	v_mov_b32_e32 v119, v152
	v_mov_b32_e32 v152, v121
	v_pk_fma_f32 v[120:121], v[42:43], v[42:43], v[84:85] op_sel_hi:[1,1,0]
	v_pk_mul_f32 v[134:135], v[116:117], v[116:117]
	v_pk_fma_f32 v[12:13], v[136:137], v[136:137], v[12:13] op_sel_hi:[1,1,0]
	v_mov_b32_e32 v154, v96
	v_mov_b32_e32 v155, v98
	v_mov_b32_e32 v98, v97
	v_pk_add_f32 v[102:103], v[102:103], v[128:129]
	v_pk_fma_f32 v[96:97], v[96:97], v[96:97], v[130:131]
	v_mul_f32_e32 v139, v15, v180
	v_mul_f32_e32 v141, v15, v181
	v_mul_f32_e32 v46, v95, v95
	v_add_f32_e32 v45, v88, v148
	v_pk_mul_f32 v[132:133], v[104:105], v[104:105]
	v_mov_b32_e32 v88, v122
	v_mov_b32_e32 v138, v124
	v_mov_b32_e32 v140, v126
	v_pk_add_f32 v[106:107], v[110:111], v[106:107]
	v_pk_add_f32 v[110:111], v[112:113], v[118:119]
	v_pk_fma_f32 v[112:113], v[114:115], v[114:115], v[134:135]
	v_mov_b32_e32 v121, v20
	v_mov_b32_e32 v13, v21
	v_pk_add_f32 v[102:103], v[102:103], v[142:143]
	v_pk_add_f32 v[96:97], v[96:97], v[96:97] op_sel:[0,1] op_sel_hi:[1,0]
	v_mul_f32_e32 v108, v15, v108
	v_pk_fma_f32 v[144:145], v[94:95], v[94:95], v[46:47] op_sel_hi:[1,1,0]
	v_pk_mul_f32 v[146:147], v[122:123], v[122:123]
	v_mov_b32_e32 v156, v100
	v_mov_b32_e32 v157, v104
	v_mov_b32_e32 v104, v101
	v_mov_b32_e32 v158, v114
	v_mov_b32_e32 v159, v116
	v_mov_b32_e32 v116, v115
	v_pk_fma_f32 v[100:101], v[100:101], v[100:101], v[132:133]
	v_pk_add_f32 v[88:89], v[122:123], v[88:89]
	v_pk_add_f32 v[114:115], v[124:125], v[138:139]
	v_pk_add_f32 v[118:119], v[126:127], v[140:141]
	v_pk_add_f32 v[106:107], v[106:107], v[150:151]
	v_pk_add_f32 v[12:13], v[120:121], v[12:13]
	v_pk_add_f32 v[112:113], v[112:113], v[112:113] op_sel:[0,1] op_sel_hi:[1,0]
	v_mov_b32_e32 v97, v226
	v_pk_mov_b32 v[22:23], v[102:103], v[22:23] op_sel:[1,0]
	v_mov_b32_e32 v195, v14
	v_add_f32_e32 v202, v45, v149
	v_mov_b32_e32 v145, v108
	v_pk_add_f32 v[100:101], v[100:101], v[100:101] op_sel:[0,1] op_sel_hi:[1,0]
	v_mov_b32_e32 v147, v89
	v_pk_mul_f32 v[120:121], v[114:115], v[114:115]
	v_pk_mul_f32 v[128:129], v[118:119], v[118:119]
	v_mov_b32_e32 v118, v115
	v_pk_mul_f32 v[114:115], v[102:103], v[102:103]
	v_pk_mul_f32 v[132:133], v[106:107], v[106:107]
	v_mov_b32_e32 v113, v108
	v_mov_b32_e32 v108, v106
	v_pk_add_f32 v[96:97], v[12:13], v[96:97]
	v_pk_mul_f32 v[12:13], v[14:15], v[22:23] op_sel_hi:[0,1]
	v_mov_b32_e32 v14, v106
	v_mov_b32_e32 v203, v15
	v_mov_b32_e32 v44, v64
	v_mov_b32_e32 v16, v68
	v_mov_b32_e32 v17, v69
	v_mov_b32_e32 v10, v65
; #define LAS __attribute__((address_space(3)))
; __device__ __forceinline__ void p7_final(const Params& p, Frame& F) {
;     ...
;         float s = 0.f;
; #pragma unroll
;         for (int i = 0; i < 8; ++i) s += (v[i][0] * v[i][0] + v[i][1] * v[i][1]) + (v[i][2] * v[i][2] + v[i][3] * v[i][3]);
;         const float rs = 1.0f / sqrtf(wave_sum(s) * (1.0f / DM) + EPS);
;         int fo = 8 * lane; asm volatile("" : "+v"(fo));
; #pragma unroll
;         for (int i = 0; i < 4; ++i) {
;             const f32x4 w0 = *(const LAS f32x4*)(fwl + 512 * i + fo), w1 = *(const LAS f32x4*)(fwl + 512 * i + fo + 4);
;             *(f32x4*)(p.out + (size_t)t * DM + 512 * i + 8 * lane) = v[2 * i] * rs * w0; *(f32x4*)(p.out + (size_t)t * DM + 512 * i + 8 * lane + 4) = v[2 * i + 1] * rs * w1; }
; #pragma unroll
;         for (int i = 0; i < 8; ++i) v[i] = nv[i];
;         me = nme; mp = nmp; mg = nmg;
;     }
	v_mov_b32_e32 v11, v66
	v_mov_b32_e32 v24, v60
	v_mov_b32_e32 v86, v61
	v_mov_b32_e32 v26, v62
	v_mov_b32_e32 v87, v63
	ds_read_b128 v[48:51], v41 offset:16384
	ds_read_b128 v[52:55], v41 offset:16400
	ds_read_b128 v[56:59], v41 offset:18432
	ds_read_b128 v[60:63], v41 offset:18448
	ds_read_b128 v[64:67], v41 offset:20480
	ds_read_b128 v[68:71], v41 offset:20496
	ds_read_b128 v[72:75], v41 offset:22528
	ds_read_b128 v[90:93], v41 offset:22544
	v_mov_b32_e32 v41, v109
	v_mov_b32_e32 v20, v40
	v_mov_b32_e32 v40, v202
	v_mov_b32_e32 v194, v103
	v_mov_b32_e32 v88, v133
	v_mov_b32_e32 v101, v13
	v_mov_b32_e32 v115, v97
	v_pk_fma_f32 v[108:109], v[14:15], v[108:109], v[146:147]
	v_mov_b64_e32 v[12:13], v[32:33]
	v_pk_add_f32 v[110:111], v[110:111], v[152:153]
	v_pk_fma_f32 v[40:41], v[202:203], v[40:41], v[88:89]
	v_mov_b64_e32 v[14:15], v[34:35]
	v_pk_add_f32 v[32:33], v[96:97], v[100:101]
	v_pk_fma_f32 v[22:23], v[194:195], v[22:23], v[114:115]
	v_pk_mul_f32 v[134:135], v[110:111], v[110:111]
	v_pk_add_f32 v[34:35], v[108:109], v[40:41]
	v_pk_mul_f32 v[40:41], v[108:109], v[40:41]
	v_pk_add_f32 v[32:33], v[32:33], v[112:113]
	v_pk_add_f32 v[22:23], v[22:23], v[144:145]
	v_mov_b32_e32 v123, v106
	v_mov_b32_e32 v130, v107
	v_pk_fma_f32 v[106:107], v[124:125], v[124:125], v[134:135]
	v_pk_fma_f32 v[132:133], v[126:127], v[126:127], v[134:135] op_sel:[0,0,1] op_sel_hi:[1,1,0]
	v_mov_b32_e32 v35, v41
	v_pk_add_f32 v[40:41], v[32:33], v[22:23]
	v_pk_mul_f32 v[22:23], v[32:33], v[22:23]
	v_mov_b32_e32 v107, v121
	v_mov_b32_e32 v133, v129
	v_mov_b32_e32 v41, v23
	v_pk_add_f32 v[88:89], v[106:107], v[132:133]
	v_pk_add_f32 v[22:23], v[40:41], v[34:35]
	v_mov_b32_e32 v108, v33
	v_pk_add_f32 v[22:23], v[22:23], v[88:89]
	s_mov_b32 s14, s2
	v_add_f32_e32 v21, v22, v23
	ds_bpermute_b32 v22, v220, v21
	v_mov_b32_e32 v131, v202
	v_mov_b32_e32 v125, v110
	v_mov_b32_e32 v127, v111
	s_and_b64 s[0:1], s[0:1], exec
	s_waitcnt lgkmcnt(0)
	v_add_f32_e32 v21, v21, v22
	ds_bpermute_b32 v22, v221, v21
	s_waitcnt lgkmcnt(0)
	v_add_f32_e32 v21, v21, v22
	ds_bpermute_b32 v22, v222, v21
	s_waitcnt lgkmcnt(0)
	v_add_f32_e32 v21, v21, v22
	ds_bpermute_b32 v22, v223, v21
	s_waitcnt lgkmcnt(0)
	v_add_f32_e32 v21, v21, v22
	ds_bpermute_b32 v22, v224, v21
	s_waitcnt lgkmcnt(0)
	v_add_f32_e32 v21, v21, v22
	ds_bpermute_b32 v22, v225, v21
	s_waitcnt lgkmcnt(0)
	v_add_f32_e32 v21, v21, v22
	v_fmamk_f32 v21, v21, 0x3a000000, v218
	v_mul_f32_e32 v22, 0x4f800000, v21
	v_cmp_gt_f32_e32 vcc, s22, v21
	s_nop 1
	v_cndmask_b32_e32 v21, v21, v22, vcc
	v_sqrt_f32_e32 v22, v21
	s_nop 0
	v_add_u32_e32 v23, -1, v22
	v_add_u32_e32 v32, 1, v22
	v_fma_f32 v33, -v23, v22, v21
	v_fma_f32 v34, -v32, v22, v21
	v_cmp_ge_f32_e64 s[2:3], 0, v33
	s_nop 1
	v_cndmask_b32_e64 v22, v22, v23, s[2:3]
	v_cmp_lt_f32_e64 s[2:3], 0, v34
	s_nop 1
	v_cndmask_b32_e64 v22, v22, v32, s[2:3]
	v_mul_f32_e32 v23, 0x37800000, v22
	v_cndmask_b32_e32 v22, v22, v23, vcc
	v_cmp_class_f32_e32 vcc, v21, v219
	s_nop 1
	v_cndmask_b32_e32 v21, v22, v21, vcc
	v_div_scale_f32 v22, s[2:3], v21, v21, 1.0
	v_rcp_f32_e32 v32, v22
	v_div_scale_f32 v23, vcc, 1.0, v21, 1.0
	v_fma_f32 v33, -v22, v32, 1.0
	v_fmac_f32_e32 v32, v33, v32
	v_mul_f32_e32 v33, v23, v32
	v_fma_f32 v34, -v22, v33, v23
	v_fmac_f32_e32 v33, v34, v32
	v_fma_f32 v22, -v22, v33, v23
	v_div_fmas_f32 v22, v22, v32, v33
	v_div_fixup_f32 v22, v22, v21, 1.0
	v_pk_mul_f32 v[32:33], v[42:43], v[22:23] op_sel_hi:[1,0]
	v_pk_mul_f32 v[34:35], v[136:137], v[22:23] op_sel_hi:[1,0]
	v_pk_mul_f32 v[40:41], v[154:155], v[22:23] op_sel_hi:[1,0]
	v_pk_mul_f32 v[42:43], v[98:99], v[22:23] op_sel_hi:[1,0]
	v_pk_mul_f32 v[88:89], v[156:157], v[22:23] op_sel_hi:[1,0]
	v_pk_mul_f32 v[96:97], v[104:105], v[22:23] op_sel_hi:[1,0]
	v_pk_mul_f32 v[98:99], v[158:159], v[22:23] op_sel_hi:[1,0]
	v_pk_mul_f32 v[100:101], v[116:117], v[22:23] op_sel_hi:[1,0]
	v_pk_mul_f32 v[102:103], v[102:103], v[22:23] op_sel_hi:[1,0]
	v_pk_mul_f32 v[94:95], v[94:95], v[22:23] op_sel_hi:[1,0]
	v_pk_mul_f32 v[104:105], v[122:123], v[22:23] op_sel_hi:[1,0]
	v_pk_mul_f32 v[106:107], v[130:131], v[22:23] op_sel_hi:[1,0]
	v_pk_mul_f32 v[110:111], v[124:125], v[22:23] op_sel_hi:[1,0]
	v_pk_mul_f32 v[112:113], v[126:127], v[22:23] op_sel_hi:[1,0]
	v_pk_mul_f32 v[108:109], v[108:109], v[22:23] op_sel_hi:[1,0]
	v_pk_mul_f32 v[22:23], v[118:119], v[22:23] op_sel_hi:[1,0]
	v_pk_mul_f32 v[34:35], v[50:51], v[34:35]
	v_pk_mul_f32 v[32:33], v[48:49], v[32:33]
	v_pk_mul_f32 v[42:43], v[54:55], v[42:43]
	v_pk_mul_f32 v[40:41], v[52:53], v[40:41]
	v_pk_mul_f32 v[50:51], v[58:59], v[96:97]
	v_pk_mul_f32 v[48:49], v[56:57], v[88:89]
	v_pk_mul_f32 v[54:55], v[62:63], v[100:101]
	v_pk_mul_f32 v[52:53], v[60:61], v[98:99]
	v_pk_mul_f32 v[58:59], v[66:67], v[94:95]
	v_pk_mul_f32 v[56:57], v[64:65], v[102:103]
	v_pk_mul_f32 v[62:63], v[70:71], v[106:107]
	v_pk_mul_f32 v[60:61], v[68:69], v[104:105]
	v_pk_mul_f32 v[66:67], v[112:113], v[74:75]
	v_pk_mul_f32 v[64:65], v[110:111], v[72:73]
	v_pk_mul_f32 v[70:71], v[22:23], v[92:93]
	v_pk_mul_f32 v[68:69], v[108:109], v[90:91]
	global_store_dwordx4 v[80:81], v[32:35], off offset:-4096
	global_store_dwordx4 v[80:81], v[40:43], off offset:-4080
	global_store_dwordx4 v[80:81], v[48:51], off offset:-2048
	global_store_dwordx4 v[80:81], v[52:55], off offset:-2032
	global_store_dwordx4 v[80:81], v[56:59], off
	global_store_dwordx4 v[80:81], v[60:63], off offset:16
	global_store_dwordx4 v[80:81], v[64:67], off offset:2048
	global_store_dwordx4 v[80:81], v[68:71], off offset:2064
	v_lshl_add_u64 v[80:81], v[80:81], 0, s[12:13]
	s_mov_b64 vcc, s[0:1]
	s_cbranch_vccnz .LBB0_1073
